# baseline (speedup 1.0000x reference)
.Lk4_st6_8:
	s_add_u32 s52, s10, 0x800000
	s_addc_u32 s53, s11, 0
	v_lshlrev_b32_e32 v169, 2, v94
	v_readfirstlane_b32 s14, v118
	s_mov_b32 m0, s14
	s_nop 0
	global_load_lds_dwordx4 v169, s[52:53] nt
	v_lshlrev_b32_e32 v169, 2, v96
	v_readfirstlane_b32 s14, v90
	s_mov_b32 m0, s14
	s_nop 0
	global_load_lds_dwordx4 v169, s[52:53] nt
	v_mfma_f32_16x16x32_f16 a[0:3], v[70:73], v[82:85], a[0:3]
	ds_read_b128 v[14:17], v158
	v_mfma_f32_16x16x32_f16 a[4:7], v[70:73], v[86:89], a[4:7]
	ds_read_b128 v[18:21], v160
	v_mfma_f32_16x16x32_f16 a[12:15], v[66:69], v[82:85], a[12:15]
	ds_read_b128 v[42:45], v168
	v_mfma_f32_16x16x32_f16 a[16:19], v[66:69], v[86:89], a[16:19]
	ds_read_b128 v[38:41], v168 offset:1024
	v_mfma_f32_16x16x32_f16 a[28:31], v[58:61], v[82:85], a[28:31]
	ds_read_b128 v[34:37], v168 offset:2048
	v_mfma_f32_16x16x32_f16 a[60:63], v[58:61], v[86:89], a[60:63]
	ds_read_b128 v[30:33], v168 offset:3072
	v_mfma_f32_16x16x32_f16 a[8:11], v[54:57], v[82:85], a[8:11]
	ds_read_b128 v[26:29], v168 offset:4096
	v_mfma_f32_16x16x32_f16 a[20:23], v[54:57], v[86:89], a[20:23]
	ds_read_b128 v[22:25], v168 offset:5120
	v_mfma_f32_16x16x32_f16 a[24:27], v[46:49], v[82:85], a[24:27]
	ds_read_b128 v[10:13], v168 offset:6144
	v_mfma_f32_16x16x32_f16 a[36:39], v[46:49], v[86:89], a[36:39]
	ds_read_b128 v[6:9], v168 offset:7168
	v_mfma_f32_16x16x32_f16 a[44:47], v[50:53], v[82:85], a[44:47]
	ds_read_b128 v[2:5], v168 offset:8192
	v_mfma_f32_16x16x32_f16 a[64:67], v[50:53], v[86:89], a[64:67]
	v_mfma_f32_16x16x32_f16 a[32:35], v[62:65], v[82:85], a[32:35]
	v_mfma_f32_16x16x32_f16 a[40:43], v[62:65], v[86:89], a[40:43]
	v_mfma_f32_16x16x32_f16 a[48:51], v[74:77], v[82:85], a[48:51]
	v_mfma_f32_16x16x32_f16 a[52:55], v[74:77], v[86:89], a[52:55]
	v_mfma_f32_16x16x32_f16 a[56:59], v[78:81], v[82:85], a[56:59]
	v_mfma_f32_16x16x32_f16 a[68:71], v[78:81], v[86:89], a[68:71]
	s_waitcnt lgkmcnt(8)
	v_mfma_f32_16x16x32_f16 a[0:3], v[42:45], v[14:17], a[0:3]
	ds_read_b128 v[82:85], v159
	v_mfma_f32_16x16x32_f16 a[4:7], v[42:45], v[18:21], a[4:7]
	ds_read_b128 v[86:89], v161
	s_waitcnt lgkmcnt(9)
	v_mfma_f32_16x16x32_f16 a[12:15], v[38:41], v[14:17], a[12:15]
	ds_read_b128 v[70:73], v168 offset:9216
	v_mfma_f32_16x16x32_f16 a[16:19], v[38:41], v[18:21], a[16:19]
	ds_read_b128 v[66:69], v168 offset:10240
	s_waitcnt lgkmcnt(10)
	v_mfma_f32_16x16x32_f16 a[28:31], v[34:37], v[14:17], a[28:31]
	ds_read_b128 v[58:61], v168 offset:11264
	v_mfma_f32_16x16x32_f16 a[60:63], v[34:37], v[18:21], a[60:63]
	ds_read_b128 v[54:57], v168 offset:12288
	s_waitcnt lgkmcnt(11)
	v_mfma_f32_16x16x32_f16 a[8:11], v[30:33], v[14:17], a[8:11]
	ds_read_b128 v[46:49], v168 offset:13312
	v_mfma_f32_16x16x32_f16 a[20:23], v[30:33], v[18:21], a[20:23]
	ds_read_b128 v[50:53], v168 offset:14336
	s_waitcnt lgkmcnt(12)
	v_mfma_f32_16x16x32_f16 a[24:27], v[26:29], v[14:17], a[24:27]
	ds_read_b128 v[62:65], v168 offset:15360
	v_mfma_f32_16x16x32_f16 a[36:39], v[26:29], v[18:21], a[36:39]
	ds_read_b128 v[74:77], v168 offset:16384
	s_waitcnt lgkmcnt(13)
	v_mfma_f32_16x16x32_f16 a[44:47], v[22:25], v[14:17], a[44:47]
	ds_read_b128 v[78:81], v168 offset:17408
	v_mfma_f32_16x16x32_f16 a[64:67], v[22:25], v[18:21], a[64:67]
	s_waitcnt lgkmcnt(13)
	v_mfma_f32_16x16x32_f16 a[32:35], v[10:13], v[14:17], a[32:35]
	v_mfma_f32_16x16x32_f16 a[40:43], v[10:13], v[18:21], a[40:43]
	s_waitcnt lgkmcnt(12)
	v_mfma_f32_16x16x32_f16 a[48:51], v[6:9], v[14:17], a[48:51]
	v_mfma_f32_16x16x32_f16 a[52:55], v[6:9], v[18:21], a[52:55]
	s_waitcnt lgkmcnt(11)
	v_mfma_f32_16x16x32_f16 a[56:59], v[2:5], v[14:17], a[56:59]
	v_mfma_f32_16x16x32_f16 a[68:71], v[2:5], v[18:21], a[68:71]
	s_waitcnt vmcnt(2) lgkmcnt(0)
	s_barrier
	v_add_u32_e32 v169, s16, v118
	s_nop 1
	v_readfirstlane_b32 s14, v169
	s_mov_b32 m0, s14
	s_nop 0
	global_load_lds_dwordx4 v[0:1], off nt
	v_add_u32_e32 v169, s16, v90
	s_nop 1
	v_readfirstlane_b32 s14, v169
	s_mov_b32 m0, s14
	s_nop 0
	global_load_lds_dwordx4 v[106:107], off nt
	v_add_u32_e32 v169, s16, v91
	s_nop 1
	v_readfirstlane_b32 s14, v169
	s_mov_b32 m0, s14
	s_nop 0
	global_load_lds_dwordx4 v[110:111], off nt
	v_add_u32_e32 v169, s16, v119
	s_nop 1
	v_readfirstlane_b32 s14, v169
	s_mov_b32 m0, s14
	s_nop 0
	global_load_lds_dwordx4 v[114:115], off nt
	s_add_u32 s52, s10, 0x1000000
	s_addc_u32 s53, s11, 0
	v_add_u32_e32 v169, 0xe000, v91
	v_lshlrev_b32_e32 v170, 2, v98
	s_nop 0
	v_readfirstlane_b32 s14, v169
	s_mov_b32 m0, s14
	s_nop 0
	global_load_lds_dwordx4 v170, s[52:53] nt
	v_add_u32_e32 v169, 0xe000, v119
	v_lshlrev_b32_e32 v170, 2, v100
	s_nop 0
	v_readfirstlane_b32 s14, v169
	s_mov_b32 m0, s14
	s_nop 0
	global_load_lds_dwordx4 v170, s[52:53] nt
	v_mfma_f32_16x16x32_f16 a[0:3], v[70:73], v[82:85], a[0:3]
	ds_read_b128 v[14:17], v160
	v_mfma_f32_16x16x32_f16 a[4:7], v[70:73], v[86:89], a[4:7]
	ds_read_b128 v[18:21], v162
	v_mfma_f32_16x16x32_f16 a[12:15], v[66:69], v[82:85], a[12:15]
	ds_read_b128 v[42:45], v164
	v_mfma_f32_16x16x32_f16 a[16:19], v[66:69], v[86:89], a[16:19]
	ds_read_b128 v[38:41], v164 offset:1024
	v_mfma_f32_16x16x32_f16 a[28:31], v[58:61], v[82:85], a[28:31]
	ds_read_b128 v[34:37], v164 offset:2048
	v_mfma_f32_16x16x32_f16 a[60:63], v[58:61], v[86:89], a[60:63]
	ds_read_b128 v[30:33], v164 offset:3072
	v_mfma_f32_16x16x32_f16 a[8:11], v[54:57], v[82:85], a[8:11]
	ds_read_b128 v[26:29], v164 offset:4096
	v_mfma_f32_16x16x32_f16 a[20:23], v[54:57], v[86:89], a[20:23]
	ds_read_b128 v[22:25], v164 offset:5120
	v_mfma_f32_16x16x32_f16 a[24:27], v[46:49], v[82:85], a[24:27]
	ds_read_b128 v[10:13], v164 offset:6144
	v_mfma_f32_16x16x32_f16 a[36:39], v[46:49], v[86:89], a[36:39]
	ds_read_b128 v[6:9], v164 offset:7168
	v_mfma_f32_16x16x32_f16 a[44:47], v[50:53], v[82:85], a[44:47]
	ds_read_b128 v[2:5], v164 offset:8192
	v_mfma_f32_16x16x32_f16 a[64:67], v[50:53], v[86:89], a[64:67]
	v_mfma_f32_16x16x32_f16 a[32:35], v[62:65], v[82:85], a[32:35]
	v_mfma_f32_16x16x32_f16 a[40:43], v[62:65], v[86:89], a[40:43]
	v_mfma_f32_16x16x32_f16 a[48:51], v[74:77], v[82:85], a[48:51]
	v_mfma_f32_16x16x32_f16 a[52:55], v[74:77], v[86:89], a[52:55]
	v_mfma_f32_16x16x32_f16 a[56:59], v[78:81], v[82:85], a[56:59]
	v_mfma_f32_16x16x32_f16 a[68:71], v[78:81], v[86:89], a[68:71]
	s_waitcnt lgkmcnt(8)
	v_mfma_f32_16x16x32_f16 a[0:3], v[42:45], v[14:17], a[0:3]
	ds_read_b128 v[82:85], v161
	v_mfma_f32_16x16x32_f16 a[4:7], v[42:45], v[18:21], a[4:7]
	ds_read_b128 v[86:89], v163
	s_waitcnt lgkmcnt(9)
	v_mfma_f32_16x16x32_f16 a[12:15], v[38:41], v[14:17], a[12:15]
	ds_read_b128 v[70:73], v164 offset:9216
	v_mfma_f32_16x16x32_f16 a[16:19], v[38:41], v[18:21], a[16:19]
	ds_read_b128 v[66:69], v164 offset:10240
	s_waitcnt lgkmcnt(10)
	v_mfma_f32_16x16x32_f16 a[28:31], v[34:37], v[14:17], a[28:31]
	ds_read_b128 v[58:61], v164 offset:11264
	v_mfma_f32_16x16x32_f16 a[60:63], v[34:37], v[18:21], a[60:63]
	ds_read_b128 v[54:57], v164 offset:12288
	s_waitcnt lgkmcnt(11)
	v_mfma_f32_16x16x32_f16 a[8:11], v[30:33], v[14:17], a[8:11]
	ds_read_b128 v[46:49], v164 offset:13312
	v_mfma_f32_16x16x32_f16 a[20:23], v[30:33], v[18:21], a[20:23]
	ds_read_b128 v[50:53], v164 offset:14336
	s_waitcnt lgkmcnt(12)
	v_mfma_f32_16x16x32_f16 a[24:27], v[26:29], v[14:17], a[24:27]
	ds_read_b128 v[62:65], v164 offset:15360
	v_mfma_f32_16x16x32_f16 a[36:39], v[26:29], v[18:21], a[36:39]
	ds_read_b128 v[74:77], v164 offset:16384
	s_waitcnt lgkmcnt(13)
	v_mfma_f32_16x16x32_f16 a[44:47], v[22:25], v[14:17], a[44:47]
	ds_read_b128 v[78:81], v164 offset:17408
	v_mfma_f32_16x16x32_f16 a[64:67], v[22:25], v[18:21], a[64:67]
	s_waitcnt lgkmcnt(13)
	v_mfma_f32_16x16x32_f16 a[32:35], v[10:13], v[14:17], a[32:35]
	v_mfma_f32_16x16x32_f16 a[40:43], v[10:13], v[18:21], a[40:43]
	s_waitcnt lgkmcnt(12)
	v_mfma_f32_16x16x32_f16 a[48:51], v[6:9], v[14:17], a[48:51]
	v_mfma_f32_16x16x32_f16 a[52:55], v[6:9], v[18:21], a[52:55]
	s_waitcnt lgkmcnt(11)
	v_mfma_f32_16x16x32_f16 a[56:59], v[2:5], v[14:17], a[56:59]
	v_mfma_f32_16x16x32_f16 a[68:71], v[2:5], v[18:21], a[68:71]
	s_waitcnt lgkmcnt(8)
	v_mfma_f32_16x16x32_f16 a[0:3], v[70:73], v[82:85], a[0:3]
	v_mfma_f32_16x16x32_f16 a[4:7], v[70:73], v[86:89], a[4:7]
	s_waitcnt lgkmcnt(9)
	v_mfma_f32_16x16x32_f16 a[12:15], v[66:69], v[82:85], a[12:15]
	v_mfma_f32_16x16x32_f16 a[16:19], v[66:69], v[86:89], a[16:19]
	s_waitcnt lgkmcnt(10)
	v_mfma_f32_16x16x32_f16 a[28:31], v[58:61], v[82:85], a[28:31]
	v_mfma_f32_16x16x32_f16 a[60:63], v[58:61], v[86:89], a[60:63]
	s_waitcnt lgkmcnt(11)
	v_mfma_f32_16x16x32_f16 a[8:11], v[54:57], v[82:85], a[8:11]
	v_mfma_f32_16x16x32_f16 a[20:23], v[54:57], v[86:89], a[20:23]
	s_waitcnt lgkmcnt(12)
	v_mfma_f32_16x16x32_f16 a[24:27], v[46:49], v[82:85], a[24:27]
	v_mfma_f32_16x16x32_f16 a[36:39], v[46:49], v[86:89], a[36:39]
	s_waitcnt lgkmcnt(13)
	v_mfma_f32_16x16x32_f16 a[44:47], v[50:53], v[82:85], a[44:47]
	v_mfma_f32_16x16x32_f16 a[64:67], v[50:53], v[86:89], a[64:67]
	s_waitcnt lgkmcnt(13)
	v_mfma_f32_16x16x32_f16 a[32:35], v[62:65], v[82:85], a[32:35]
	v_mfma_f32_16x16x32_f16 a[40:43], v[62:65], v[86:89], a[40:43]
	s_waitcnt lgkmcnt(12)
	v_mfma_f32_16x16x32_f16 a[48:51], v[74:77], v[82:85], a[48:51]
	v_mfma_f32_16x16x32_f16 a[52:55], v[74:77], v[86:89], a[52:55]
	s_waitcnt lgkmcnt(11)
	v_mfma_f32_16x16x32_f16 a[56:59], v[78:81], v[82:85], a[56:59]
	v_mfma_f32_16x16x32_f16 a[68:71], v[78:81], v[86:89], a[68:71]
	s_waitcnt lgkmcnt(0)
	s_setprio 0
.LBB3_32:
	s_barrier
	s_add_u32 s52, s10, 0x1000000
	s_addc_u32 s53, s11, 0
	v_add_u32_e32 v61, 0xe000, v118
	v_lshlrev_b32_e32 v62, 2, v94
	s_nop 0
	v_readfirstlane_b32 s44, v61
	s_mov_b32 m0, s44
	s_nop 0
	global_load_lds_dwordx4 v62, s[52:53] nt
	v_add_u32_e32 v61, 0xe000, v90
	v_lshlrev_b32_e32 v62, 2, v96
	s_nop 0
	v_readfirstlane_b32 s44, v61
	s_mov_b32 m0, s44
	s_nop 0
	global_load_lds_dwordx4 v62, s[52:53] nt
	v_mbcnt_lo_u32_b32 v63, -1, 0
	v_mbcnt_hi_u32_b32 v63, -1, v63
	v_lshlrev_b32_e32 v63, 4, v63
	v_add_u32_e32 v64, v91, v63
	v_add_u32_e32 v65, v119, v63
	v_add_u32_e32 v66, v118, v63
	v_add_u32_e32 v67, v90, v63
	ds_write_b128 v64, v[128:131]
	ds_write_b128 v65, v[132:135]
	ds_write_b128 v66, v[172:175] offset:28672
	ds_write_b128 v67, v[176:179] offset:28672
	ds_write_b128 v64, v[140:143] offset:28672
	ds_write_b128 v65, v[144:147] offset:28672
	v_lshl_add_u32 v0, v120, 5, s22
	v_or_b32_e32 v1, s23, v121
	s_movk_i32 s0, 0x7f
	v_lshl_or_b32 v7, v93, 1, v0
	s_movk_i32 s1, 0x7e
	s_nop 15
	s_nop 15
	v_cmp_eq_u32_e64 s[4:5], s1, v7
	s_nop 7
	v_cmp_gt_u32_e32 vcc, s0, v1
	v_accvgpr_read_b32 v5, a14
	v_cmp_eq_u32_e64 s[0:1], 0, v1
	v_or_b32_e32 v4, v93, v7
	v_cmp_eq_u32_e64 s[2:3], 0, v4
	v_cndmask_b32_e64 v14, v5, 0, s[0:1]
	v_accvgpr_read_b32 v5, a13
	v_cndmask_b32_e64 v22, v5, 0, s[0:1]
	v_accvgpr_read_b32 v5, a12
	v_cndmask_b32_e64 v116, v5, 0, s[0:1]
	v_accvgpr_read_b32 v5, a49
	v_cndmask_b32_e32 v16, 0, v5, vcc
	v_accvgpr_read_b32 v5, a48
	v_cndmask_b32_e32 v28, 0, v5, vcc
	v_accvgpr_read_b32 v5, a30
	v_cndmask_b32_e64 v10, v5, 0, s[0:1]
	v_accvgpr_read_b32 v5, a29
	v_cndmask_b32_e64 v24, v5, 0, s[0:1]
	v_accvgpr_read_b32 v5, a28
	v_cndmask_b32_e64 v42, v5, 0, s[0:1]
	v_accvgpr_read_b32 v5, a57
	v_cndmask_b32_e32 v20, 0, v5, vcc
	v_accvgpr_read_b32 v5, a56
	v_cndmask_b32_e32 v38, 0, v5, vcc
	v_accvgpr_read_b32 v5, a6
	v_cndmask_b32_e64 v15, v5, 0, s[0:1]
	v_accvgpr_read_b32 v5, a5
	v_cndmask_b32_e64 v23, v5, 0, s[0:1]
	v_accvgpr_read_b32 v5, a4
	v_cndmask_b32_e64 v117, v5, 0, s[0:1]
	v_accvgpr_read_b32 v5, a41
	v_cndmask_b32_e32 v17, 0, v5, vcc
	v_accvgpr_read_b32 v5, a40
	v_cndmask_b32_e32 v29, 0, v5, vcc
	v_accvgpr_read_b32 v5, a17
	v_cndmask_b32_e64 v37, v5, 0, s[0:1]
	v_accvgpr_read_b32 v5, a16
	v_cndmask_b32_e64 v47, v5, 0, s[0:1]
	v_accvgpr_read_b32 v5, a52
	v_cndmask_b32_e32 v45, 0, v5, vcc
	v_accvgpr_read_b32 v5, a68
	v_cndmask_b32_e32 v12, 0, v5, vcc
	v_accvgpr_read_b32 v5, a0
	s_or_b64 s[8:9], s[2:3], s[0:1]
	v_cmp_eq_u32_e64 s[6:7], 15, v93
	v_accvgpr_read_b32 v11, a8
	v_cndmask_b32_e64 v112, v5, 0, s[8:9]
	v_accvgpr_read_b32 v4, a67
	v_mov_b32_e32 v5, 0x90
	s_and_b64 s[4:5], s[6:7], s[4:5]
	v_mov_b64_e32 v[40:41], v[16:17]
	v_cndmask_b32_e64 v16, v11, 0, s[2:3]
	v_cndmask_b32_e64 v11, 12, v5, s[6:7]
	v_cndmask_b32_e64 v61, v4, 0, s[4:5]
	v_accvgpr_read_b32 v4, a61
	s_or_b64 s[6:7], s[4:5], s[0:1]
	v_cndmask_b32_e64 v87, v4, 0, s[6:7]
	v_accvgpr_read_b32 v4, a60
	v_cndmask_b32_e64 v86, v4, 0, s[6:7]
	v_accvgpr_read_b32 v4, a65
	v_cndmask_b32_e64 v5, v4, 0, s[4:5]
	v_accvgpr_read_b32 v4, a64
	v_cndmask_b32_e64 v4, v4, 0, s[4:5]
	s_lshl_b32 s14, s18, 2
	v_mov_b64_e32 v[32:33], v[4:5]
	v_lshl_or_b32 v4, v122, 18, s14
	v_mov_b32_e32 v5, 0
	v_mov_b64_e32 v[62:63], v[14:15]
	v_lshl_add_u64 v[14:15], s[12:13], 0, v[4:5]
	v_lshlrev_b32_e32 v4, 7, v1
	v_lshl_add_u64 v[14:15], v[4:5], 2, v[14:15]
	v_lshlrev_b32_e32 v4, 2, v7
	v_mul_u32_u24_e32 v1, 24, v122
	v_lshl_add_u64 v[54:55], v[14:15], 0, v[4:5]
	v_mbcnt_lo_u32_b32 v138, -1, 0
	v_mbcnt_hi_u32_b32 v138, -1, v138
	v_and_b32_e32 v138, 1, v138
	v_mul_u32_u24_e32 v138, 0xfff8, v138
	v_add_u32_e32 v138, 0xffff0000, v138
	v_mov_b32_e32 v139, -1
	v_lshl_add_u64 v[134:135], v[54:55], 0, v[138:139]
	s_mov_b32 s28, 0x55555555
	s_mov_b32 s29, 0x55555555
	s_mov_b32 s30, 0xaaaaaaaa
	s_mov_b32 s31, 0xaaaaaaaa
	v_or_b32_e32 v1, v1, v121
	v_lshlrev_b32_e32 v4, 7, v120
	s_movk_i32 s12, 0x120
	v_mad_u32_u24 v1, v1, s12, v4
	s_add_u32 s12, s10, 0x800000
	v_accvgpr_read_b32 v7, a72
	v_mov_b64_e32 v[80:81], v[28:29]
	s_addc_u32 s13, s11, 0
	v_lshlrev_b64 v[28:29], 2, v[94:95]
	v_readfirstlane_b32 s14, v7
	v_add_u32_e32 v7, 0, v90
	v_lshl_add_u64 v[4:5], s[12:13], 0, v[28:29]
	s_mov_b32 m0, s14
	v_lshlrev_b64 v[30:31], 2, v[96:97]
	v_readfirstlane_b32 s14, v7
	v_mov_b32_e32 v14, v7
	v_add_u32_e32 v7, 0, v91
	s_waitcnt lgkmcnt(0)
	v_lshlrev_b64 v[56:57], 2, v[98:99]
	v_mov_b32_e32 v19, v7
	v_lshlrev_b64 v[58:59], 2, v[100:101]
	v_add_u32_e32 v7, 0, v119
	v_accvgpr_read_b32 v25, a72
	v_mov_b32_e32 v21, v7
	v_lshl_add_u32 v15, v93, 3, v1
	v_add_u32_e32 v1, v1, v11
	s_waitcnt vmcnt(16)
	v_accvgpr_write_b32 a12, v14
	v_mov_b64_e32 v[124:125], v[56:57]
	v_accvgpr_write_b32 a13, v19
	v_mov_b64_e32 v[126:127], v[58:59]
	v_accvgpr_write_b32 a16, v21
	s_waitcnt lgkmcnt(0)
	s_barrier
	v_add_u32_e32 v14, 0x16010, v15
	v_mov_b32_e32 v122, v15
	v_add_u32_e32 v15, 0x16000, v1
	ds_read_b64 v[64:65], v14
	ds_read_b64 v[66:67], v14 offset:288
	ds_read_b64 v[68:69], v14 offset:576
	ds_read_b64 v[76:77], v14 offset:1728
	ds_read_b64 v[78:79], v14 offset:2016
	ds_read_b64 v[4:5], v14 offset:2304
	ds_read_b64 v[84:85], v14 offset:3456
	ds_read_b64 v[74:75], v14 offset:3744
	ds_read_b64 v[88:89], v14 offset:4032
	ds_read_b64 v[100:101], v14 offset:5184
	ds_read_b64 v[106:107], v14 offset:5472
	ds_read_b64 v[120:121], v14 offset:5760
	ds_read_b32 v43, v15
	ds_read_b32 v19, v15 offset:288
	ds_read_b32 v39, v15 offset:576
	ds_read_b32 v25, v15 offset:1728
	ds_read_b32 v7, v15 offset:2016
	ds_read_b32 v21, v15 offset:2304
	ds_read_b32 v11, v15 offset:3456
	ds_read_b32 v35, v15 offset:3744
	ds_read_b32 v59, v15 offset:4032
	ds_read_b32 v57, v15 offset:5184
	ds_read_b32 v51, v15 offset:5472
	ds_read_b32 v49, v15 offset:5760
	s_waitcnt lgkmcnt(0)
	v_accvgpr_read_b32 v8, a26
	v_mov_b32_e32 v46, v43
	v_mov_b32_e32 v113, v65
	v_mov_b32_e32 v26, v19
	v_mov_b32_dpp v46, v65 row_shr:1 row_mask:0xf bank_mask:0xf
	v_pk_mul_f32 v[70:71], v[112:113], v[46:47]
	v_accvgpr_read_b32 v9, a22
	v_accvgpr_read_b32 v27, a36
	v_mov_b32_dpp v43, v64 row_shl:1 row_mask:0xf bank_mask:0xf
	v_mov_b32_dpp v26, v67 row_shr:1 row_mask:0xf bank_mask:0xf
	v_pk_fma_f32 v[70:71], v[64:65], v[116:117], v[70:71] op_sel_hi:[0,1,1]
	v_pk_mov_b32 v[64:65], v[64:65], v[86:87] op_sel:[1,0]
	v_mov_b32_e32 v17, v67
	v_mov_b64_e32 v[102:103], v[8:9]
	v_accvgpr_read_b32 v8, a25
	v_accvgpr_read_b32 v114, a24
	v_accvgpr_read_b32 v9, a21
	v_accvgpr_read_b32 v115, a20
	v_accvgpr_read_b32 v2, a32
	v_mov_b64_e32 v[82:83], v[30:31]
	v_pk_fma_f32 v[70:71], v[64:65], v[42:43], v[70:71]
	v_pk_mul_f32 v[64:65], v[16:17], v[26:27]
	v_mov_b64_e32 v[30:31], v[32:33]
	v_accvgpr_read_b32 v18, a44
	v_mov_b64_e32 v[104:105], v[8:9]
	v_cndmask_b32_e32 v9, 0, v2, vcc
	v_accvgpr_write_b32 a4, v14
	v_mov_b32_dpp v19, v66 row_shl:1 row_mask:0xf bank_mask:0xf
	v_pk_fma_f32 v[64:65], v[66:67], v[114:115], v[64:65] op_sel_hi:[0,1,1]
	v_pk_mov_b32 v[66:67], v[66:67], v[30:31] op_sel:[1,0]
	v_accvgpr_read_b32 v14, a69
	v_mov_b32_e32 v44, v39
	v_mov_b32_e32 v60, v1
	v_pk_fma_f32 v[66:67], v[66:67], v[18:19], v[64:65]
	v_cndmask_b32_e32 v14, 0, v14, vcc
	v_cndmask_b32_e64 v0, v9, 0, s[2:3]
	v_mov_b32_dpp v44, v69 row_shr:1 row_mask:0xf bank_mask:0xf
	v_pk_add_f32 v[70:71], v[70:71], 0 op_sel_hi:[1,0]
	v_mov_b32_e32 v1, v69
	v_accvgpr_write_b32 a0, v15
	v_cndmask_b32_e64 v15, v14, 0, s[4:5]
	v_cndmask_b32_e64 v14, v12, 0, s[4:5]
	v_pk_add_f32 v[66:67], v[70:71], v[66:67]
	v_pk_mul_f32 v[70:71], v[0:1], v[44:45]
	v_mov_b32_dpp v39, v68 row_shl:1 row_mask:0xf bank_mask:0xf
	v_pk_fma_f32 v[70:71], v[68:69], v[80:81], v[70:71] op_sel_hi:[0,1,1]
	v_pk_mov_b32 v[68:69], v[68:69], v[14:15] op_sel:[1,0]
	v_accvgpr_read_b32 v9, a1
	v_pk_fma_f32 v[68:69], v[68:69], v[38:39], v[70:71]
	v_mov_b32_e32 v36, v25
	v_cndmask_b32_e64 v64, v9, 0, s[8:9]
	v_pk_add_f32 v[66:67], v[66:67], v[68:69]
	v_mov_b32_dpp v36, v77 row_shr:1 row_mask:0xf bank_mask:0xf
	v_mov_b32_e32 v65, v77
	v_mov_b64_e32 v[108:109], v[22:23]
	v_accvgpr_read_b32 v9, a9
	v_mov_b32_e32 v128, v66
	v_mov_b32_e32 v129, v67
	v_mov_b32_e32 v12, v7
	v_pk_mul_f32 v[66:67], v[64:65], v[36:37]
	v_accvgpr_read_b32 v13, a37
	v_mov_b64_e32 v[72:73], v[28:29]
	v_cndmask_b32_e64 v28, v9, 0, s[2:3]
	v_mov_b32_dpp v25, v76 row_shl:1 row_mask:0xf bank_mask:0xf
	v_mov_b32_dpp v12, v79 row_shr:1 row_mask:0xf bank_mask:0xf
	v_pk_fma_f32 v[66:67], v[76:77], v[108:109], v[66:67] op_sel_hi:[0,1,1]
	v_mov_b32_e32 v76, v77
	v_mov_b32_e32 v77, v87
	v_mov_b32_e32 v29, v79
	v_pk_fma_f32 v[66:67], v[76:77], v[24:25], v[66:67]
	v_pk_mul_f32 v[76:77], v[28:29], v[12:13]
	v_accvgpr_read_b32 v6, a45
	v_accvgpr_read_b32 v2, a33
	v_mov_b32_dpp v7, v78 row_shl:1 row_mask:0xf bank_mask:0xf
	v_pk_fma_f32 v[76:77], v[78:79], v[104:105], v[76:77] op_sel_hi:[0,1,1]
	v_mov_b32_e32 v78, v79
	v_mov_b32_e32 v79, v31
	v_cndmask_b32_e32 v2, 0, v2, vcc
	v_accvgpr_read_b32 v50, a53
	v_pk_fma_f32 v[76:77], v[78:79], v[6:7], v[76:77]
	v_mov_b32_e32 v78, v21
	v_accvgpr_write_b32 a44, v80
	v_cndmask_b32_e32 v79, 0, v50, vcc
	v_cndmask_b32_e64 v52, v2, 0, s[2:3]
	v_mov_b32_dpp v78, v5 row_shr:1 row_mask:0xf bank_mask:0xf
	v_pk_add_f32 v[66:67], v[66:67], 0 op_sel_hi:[1,0]
	v_mov_b32_e32 v53, v5
	v_accvgpr_write_b32 a45, v81
	v_accvgpr_write_b32 a21, v15
	v_pk_add_f32 v[80:81], v[66:67], v[76:77]
	v_pk_mul_f32 v[66:67], v[52:53], v[78:79]
	v_accvgpr_write_b32 a24, v40
	v_accvgpr_read_b32 v2, a2
	v_mov_b32_dpp v21, v4 row_shl:1 row_mask:0xf bank_mask:0xf
	v_pk_fma_f32 v[66:67], v[4:5], v[40:41], v[66:67] op_sel_hi:[0,1,1]
	v_accvgpr_write_b32 a25, v41
	v_mov_b32_e32 v4, v5
	v_accvgpr_read_b32 v5, a21
	v_cndmask_b32_e64 v40, v2, 0, s[8:9]
	v_accvgpr_read_b32 v2, a62
	v_accvgpr_read_b32 v8, a18
	v_accvgpr_read_b32 v48, a63
	v_accvgpr_write_b32 a20, v14
	v_accvgpr_write_b32 a41, v23
	v_pk_fma_f32 v[4:5], v[4:5], v[20:21], v[66:67]
	s_mov_b64 s[12:13], 0x10000
	v_cndmask_b32_e64 v14, v2, 0, s[6:7]
	v_mov_b32_e32 v76, v11
	v_accvgpr_read_b32 v2, a10
	v_accvgpr_write_b32 a40, v22
	v_cndmask_b32_e64 v15, v48, 0, s[6:7]
	v_cndmask_b32_e64 v77, v8, 0, s[0:1]
	v_pk_add_f32 v[4:5], v[80:81], v[4:5]
	v_lshl_add_u64 v[136:137], v[134:135], 0, s[12:13]
	v_mov_b32_dpp v76, v85 row_shr:1 row_mask:0xf bank_mask:0xf
	v_mov_b32_e32 v41, v85
	v_cndmask_b32_e64 v22, v2, 0, s[2:3]
	v_mov_b32_e32 v2, v35
	v_accvgpr_read_b32 v1, a50
	v_accvgpr_read_b32 v3, a38
	s_mov_b64 s[32:33], vcc
	s_nop 1
	s_mov_b64 vcc, s[28:29]
	s_nop 0
	v_cndmask_b32_dpp v130, v4, v128, vcc quad_perm:[1,0,3,2] row_mask:0xf bank_mask:0xf
	v_cndmask_b32_dpp v131, v5, v129, vcc quad_perm:[1,0,3,2] row_mask:0xf bank_mask:0xf
	s_mov_b64 vcc, s[30:31]
	s_nop 0
	v_cndmask_b32_dpp v132, v128, v4, vcc quad_perm:[1,0,3,2] row_mask:0xf bank_mask:0xf
	v_cndmask_b32_dpp v133, v129, v5, vcc quad_perm:[1,0,3,2] row_mask:0xf bank_mask:0xf
	global_store_dwordx4 v[136:137], v[130:133], off sc0 sc1 nt
	s_nop 1
	s_mov_b64 vcc, s[32:33]
	v_mov_b64_e32 v[8:9], v[14:15]
	v_pk_mul_f32 v[4:5], v[40:41], v[76:77]
	v_mov_b64_e32 v[66:67], v[62:63]
	v_mov_b32_dpp v2, v75 row_shr:1 row_mask:0xf bank_mask:0xf
	v_mov_b32_e32 v23, v75
	v_cndmask_b32_e32 v62, 0, v1, vcc
	v_accvgpr_read_b32 v1, a42
	v_mov_b32_dpp v11, v84 row_shl:1 row_mask:0xf bank_mask:0xf
	v_pk_fma_f32 v[4:5], v[84:85], v[66:67], v[4:5] op_sel_hi:[0,1,1]
	v_pk_mov_b32 v[80:81], v[84:85], v[8:9] op_sel:[1,0]
	v_pk_mul_f32 v[84:85], v[22:23], v[2:3]
	v_accvgpr_read_b32 v2, a58
	v_cndmask_b32_e32 v63, 0, v1, vcc
	v_accvgpr_read_b32 v1, a70
	v_pk_fma_f32 v[80:81], v[80:81], v[10:11], v[4:5]
	v_accvgpr_read_b32 v4, a66
	v_cndmask_b32_e32 v58, 0, v2, vcc
	v_cndmask_b32_e32 v1, 0, v1, vcc
	v_accvgpr_read_b32 v2, a71
	v_cndmask_b32_e64 v8, v4, 0, s[4:5]
	v_cndmask_b32_e32 v2, 0, v2, vcc
	v_cndmask_b32_e64 v4, v1, 0, s[4:5]
	v_accvgpr_read_b32 v1, a34
	v_mov_b32_e32 v9, v61
	v_cndmask_b32_e64 v5, v2, 0, s[4:5]
	v_cndmask_b32_e32 v1, 0, v1, vcc
	v_accvgpr_read_b32 v2, a54
	v_mov_b32_e32 v92, v59
	v_accvgpr_read_b32 v34, a46
	v_mov_b32_dpp v35, v74 row_shl:1 row_mask:0xf bank_mask:0xf
	v_pk_fma_f32 v[84:85], v[74:75], v[102:103], v[84:85] op_sel_hi:[0,1,1]
	v_pk_mov_b32 v[74:75], v[74:75], v[8:9] op_sel:[1,0]
	v_cndmask_b32_e32 v93, 0, v2, vcc
	v_mov_b32_dpp v92, v89 row_shr:1 row_mask:0xf bank_mask:0xf
	v_cndmask_b32_e64 v96, v1, 0, s[2:3]
	v_mov_b32_e32 v97, v89
	v_accvgpr_read_b32 v1, a31
	v_pk_fma_f32 v[74:75], v[74:75], v[34:35], v[84:85]
	v_pk_mul_f32 v[84:85], v[96:97], v[92:93]
	v_accvgpr_write_b32 a8, v62
	v_cndmask_b32_e64 v56, v1, 0, s[0:1]
	v_accvgpr_read_b32 v1, a15
	v_pk_fma_f32 v[84:85], v[88:89], v[62:63], v[84:85] op_sel_hi:[0,1,1]
	v_accvgpr_write_b32 a9, v63
	v_cndmask_b32_e64 v62, v1, 0, s[0:1]
	v_accvgpr_read_b32 v1, a7
	v_cndmask_b32_e64 v63, v1, 0, s[0:1]
	v_accvgpr_read_b32 v1, a19
	v_pk_add_f32 v[80:81], v[80:81], 0 op_sel_hi:[1,0]
	v_mov_b32_dpp v59, v88 row_shl:1 row_mask:0xf bank_mask:0xf
	v_pk_mov_b32 v[88:89], v[88:89], v[4:5] op_sel:[1,0]
	v_cndmask_b32_e64 v95, v1, 0, s[0:1]
	v_accvgpr_read_b32 v1, a3
	v_accvgpr_write_b32 a36, v104
	v_pk_add_f32 v[80:81], v[80:81], v[74:75]
	v_pk_fma_f32 v[84:85], v[88:89], v[58:59], v[84:85]
	v_mov_b32_e32 v94, v57
	v_cndmask_b32_e64 v98, v1, 0, s[8:9]
	v_accvgpr_read_b32 v1, a11
	v_accvgpr_write_b32 a37, v105
	v_accvgpr_write_b32 a32, v102
	v_pk_add_f32 v[80:81], v[80:81], v[84:85]
	s_mov_b64 s[4:5], 0x20000
	v_mov_b32_dpp v94, v101 row_shr:1 row_mask:0xf bank_mask:0xf
	v_mov_b32_e32 v99, v101
	v_cndmask_b32_e64 v104, v1, 0, s[2:3]
	v_accvgpr_read_b32 v1, a59
	v_accvgpr_write_b32 a29, v15
	v_accvgpr_write_b32 a33, v103
	v_accvgpr_write_b32 a49, v5
	v_lshl_add_u64 v[84:85], v[54:55], 0, s[4:5]
	v_mov_b32_e32 v128, v80
	v_mov_b32_e32 v129, v81
	v_pk_mul_f32 v[80:81], v[98:99], v[94:95]
	v_mov_b32_e32 v102, v51
	v_cndmask_b32_e32 v48, 0, v1, vcc
	v_accvgpr_read_b32 v1, a51
	v_accvgpr_write_b32 a48, v4
	v_mov_b32_dpp v57, v100 row_shl:1 row_mask:0xf bank_mask:0xf
	v_pk_fma_f32 v[80:81], v[100:101], v[62:63], v[80:81] op_sel_hi:[0,1,1]
	v_mov_b32_e32 v84, v101
	v_accvgpr_read_b32 v85, a29
	v_accvgpr_read_b32 v103, a39
	v_mov_b32_dpp v102, v107 row_shr:1 row_mask:0xf bank_mask:0xf
	v_mov_b32_e32 v105, v107
	v_cndmask_b32_e32 v4, 0, v1, vcc
	v_accvgpr_read_b32 v1, a43
	v_pk_fma_f32 v[80:81], v[84:85], v[56:57], v[80:81]
	v_accvgpr_read_b32 v30, a27
	v_accvgpr_read_b32 v31, a23
	v_pk_mul_f32 v[84:85], v[104:105], v[102:103]
	v_cndmask_b32_e32 v5, 0, v1, vcc
	v_accvgpr_read_b32 v1, a35
	v_accvgpr_read_b32 v50, a47
	v_mov_b32_dpp v51, v106 row_shl:1 row_mask:0xf bank_mask:0xf
	v_pk_fma_f32 v[84:85], v[106:107], v[30:31], v[84:85] op_sel_hi:[0,1,1]
	v_mov_b32_e32 v106, v107
	v_mov_b32_e32 v107, v9
	v_cndmask_b32_e32 v1, 0, v1, vcc
	v_accvgpr_read_b32 v2, a55
	v_mov_b32_e32 v108, v49
	v_pk_fma_f32 v[84:85], v[106:107], v[50:51], v[84:85]
	v_pk_add_f32 v[80:81], v[80:81], 0 op_sel_hi:[1,0]
	v_cndmask_b32_e32 v109, 0, v2, vcc
	v_mov_b32_dpp v108, v121 row_shr:1 row_mask:0xf bank_mask:0xf
	v_cndmask_b32_e64 v110, v1, 0, s[2:3]
	v_mov_b32_e32 v111, v121
	v_pk_add_f32 v[80:81], v[80:81], v[84:85]
	v_pk_mul_f32 v[84:85], v[110:111], v[108:109]
	v_mov_b32_dpp v49, v120 row_shl:1 row_mask:0xf bank_mask:0xf
	v_pk_fma_f32 v[84:85], v[120:121], v[4:5], v[84:85] op_sel_hi:[0,1,1]
	v_mov_b32_e32 v120, v121
	v_accvgpr_read_b32 v121, a49
	v_pk_fma_f32 v[84:85], v[120:121], v[48:49], v[84:85]
	s_mov_b64 s[0:1], 0x30000
	v_pk_add_f32 v[80:81], v[80:81], v[84:85]
	v_lshl_add_u64 v[136:137], v[134:135], 0, s[0:1]
	v_add_u32_e32 v1, s17, v118
	s_add_u32 s0, s10, 0x1400000
	s_mov_b64 s[32:33], vcc
	s_nop 1
	s_mov_b64 vcc, s[28:29]
	s_nop 0
	v_cndmask_b32_dpp v130, v80, v128, vcc quad_perm:[1,0,3,2] row_mask:0xf bank_mask:0xf
	v_cndmask_b32_dpp v131, v81, v129, vcc quad_perm:[1,0,3,2] row_mask:0xf bank_mask:0xf
	s_mov_b64 vcc, s[30:31]
	s_nop 0
	v_cndmask_b32_dpp v132, v128, v80, vcc quad_perm:[1,0,3,2] row_mask:0xf bank_mask:0xf
	v_cndmask_b32_dpp v133, v129, v81, vcc quad_perm:[1,0,3,2] row_mask:0xf bank_mask:0xf
	global_store_dwordx4 v[136:137], v[130:133], off sc0 sc1 nt
	s_nop 1
	s_mov_b64 vcc, s[32:33]
	v_readfirstlane_b32 s2, v1
	s_addc_u32 s1, s11, 0
	v_add_u32_e32 v1, s17, v90
	s_waitcnt vmcnt(6)
	v_lshl_add_u64 v[80:81], s[0:1], 0, v[72:73]
	s_mov_b32 m0, s2
	v_readfirstlane_b32 s2, v1
	v_mov_b64_e32 v[74:75], v[82:83]
	v_add_u32_e32 v1, s17, v91
	s_waitcnt lgkmcnt(0)
	s_barrier
	global_load_lds_dwordx4 v[80:81], off nt
	v_lshl_add_u64 v[80:81], s[0:1], 0, v[74:75]
	s_mov_b32 m0, s2
	v_readfirstlane_b32 s2, v1
	v_add_u32_e32 v1, s17, v119
	global_load_lds_dwordx4 v[80:81], off nt
	v_lshl_add_u64 v[80:81], s[0:1], 0, v[124:125]
	s_mov_b32 m0, s2
	v_readfirstlane_b32 s2, v1
	global_load_lds_dwordx4 v[80:81], off nt
	v_lshl_add_u64 v[80:81], s[0:1], 0, v[126:127]
	s_mov_b32 m0, s2
	v_accvgpr_write_b32 a53, v33
	v_accvgpr_write_b32 a2, v62
	v_accvgpr_write_b32 a7, v5
	v_accvgpr_write_b32 a22, v124
	v_accvgpr_write_b32 a30, v126
	global_load_lds_dwordx4 v[80:81], off nt
	v_accvgpr_write_b32 a52, v32
	v_accvgpr_write_b32 a3, v63
	v_accvgpr_write_b32 a6, v4
	v_mov_b64_e32 v[32:33], v[72:73]
	v_accvgpr_write_b32 a23, v125
	v_accvgpr_write_b32 a31, v127
	v_add_u32_e32 v2, 0x1d010, v122
	v_accvgpr_write_b32 a10, v122
	v_add_u32_e32 v5, 0x1d000, v60
	v_mov_b32_e32 v4, v60
	ds_read_b64 v[62:63], v2
	ds_read_b64 v[60:61], v2 offset:288
	ds_read_b64 v[72:73], v2 offset:576
	ds_read_b64 v[70:71], v2 offset:1728
	ds_read_b64 v[68:69], v2 offset:2016
	ds_read_b64 v[82:83], v2 offset:2304
	ds_read_b64 v[80:81], v2 offset:3456
	ds_read_b64 v[84:85], v2 offset:3744
	ds_read_b64 v[126:127], v2 offset:4032
	ds_read_b64 v[124:125], v2 offset:5184
	ds_read_b64 v[122:123], v2 offset:5472
	ds_read_b64 v[120:121], v2 offset:5760
	ds_read_b32 v43, v5
	ds_read_b32 v19, v5 offset:288
	ds_read_b32 v39, v5 offset:576
	ds_read_b32 v25, v5 offset:1728
	ds_read_b32 v7, v5 offset:2016
	ds_read_b32 v21, v5 offset:2304
	ds_read_b32 v11, v5 offset:3456
	ds_read_b32 v35, v5 offset:3744
	ds_read_b32 v59, v5 offset:4032
	ds_read_b32 v57, v5 offset:5184
	ds_read_b32 v51, v5 offset:5472
	ds_read_b32 v49, v5 offset:5760
	s_waitcnt lgkmcnt(0)
	v_mov_b64_e32 v[100:101], v[86:87]
	v_mov_b32_e32 v46, v43
	v_mov_b32_e32 v113, v63
	v_mov_b32_e32 v26, v19
	v_mov_b32_dpp v46, v63 row_shr:1 row_mask:0xf bank_mask:0xf
	v_pk_mul_f32 v[88:89], v[112:113], v[46:47]
	v_mov_b32_dpp v43, v62 row_shl:1 row_mask:0xf bank_mask:0xf
	v_pk_fma_f32 v[88:89], v[62:63], v[116:117], v[88:89] op_sel_hi:[0,1,1]
	v_pk_mov_b32 v[62:63], v[62:63], v[100:101] op_sel:[1,0]
	v_mov_b32_dpp v26, v61 row_shr:1 row_mask:0xf bank_mask:0xf
	v_mov_b32_e32 v17, v61
	v_pk_fma_f32 v[62:63], v[62:63], v[42:43], v[88:89]
	v_pk_mul_f32 v[88:89], v[16:17], v[26:27]
	v_accvgpr_write_b32 a34, v16
	v_accvgpr_read_b32 v16, a52
	v_accvgpr_read_b32 v17, a53
	v_mov_b32_dpp v19, v60 row_shl:1 row_mask:0xf bank_mask:0xf
	v_pk_fma_f32 v[88:89], v[60:61], v[114:115], v[88:89] op_sel_hi:[0,1,1]
	v_pk_mov_b32 v[60:61], v[60:61], v[16:17] op_sel:[1,0]
	v_mov_b32_e32 v44, v39
	v_accvgpr_write_b32 a28, v14
	v_pk_fma_f32 v[60:61], v[60:61], v[18:19], v[88:89]
	v_pk_add_f32 v[62:63], v[62:63], 0 op_sel_hi:[1,0]
	v_mov_b32_dpp v44, v73 row_shr:1 row_mask:0xf bank_mask:0xf
	v_mov_b32_e32 v1, v73
	v_accvgpr_read_b32 v14, a44
	v_accvgpr_read_b32 v89, a21
	v_pk_add_f32 v[60:61], v[62:63], v[60:61]
	v_pk_mul_f32 v[62:63], v[0:1], v[44:45]
	v_accvgpr_read_b32 v15, a45
	v_accvgpr_read_b32 v88, a20
	v_mov_b32_dpp v39, v72 row_shl:1 row_mask:0xf bank_mask:0xf
	v_pk_fma_f32 v[62:63], v[72:73], v[14:15], v[62:63] op_sel_hi:[0,1,1]
	v_pk_mov_b32 v[72:73], v[72:73], v[88:89] op_sel:[1,0]
	v_mov_b32_e32 v36, v25
	v_pk_fma_f32 v[62:63], v[72:73], v[38:39], v[62:63]
	s_mov_b64 s[0:1], 0x400000
	v_pk_add_f32 v[60:61], v[60:61], v[62:63]
	v_mov_b32_dpp v36, v71 row_shr:1 row_mask:0xf bank_mask:0xf
	v_mov_b32_e32 v65, v71
	v_accvgpr_read_b32 v87, a41
	v_lshl_add_u64 v[62:63], v[54:55], 0, s[0:1]
	v_mov_b32_e32 v128, v60
	v_mov_b32_e32 v129, v61
	v_pk_mul_f32 v[60:61], v[64:65], v[36:37]
	v_accvgpr_read_b32 v86, a40
	v_mov_b32_e32 v12, v7
	v_mov_b32_dpp v25, v70 row_shl:1 row_mask:0xf bank_mask:0xf
	v_pk_fma_f32 v[60:61], v[70:71], v[86:87], v[60:61] op_sel_hi:[0,1,1]
	v_mov_b32_e32 v62, v71
	v_mov_b32_e32 v63, v101
	v_mov_b32_dpp v12, v69 row_shr:1 row_mask:0xf bank_mask:0xf
	v_mov_b32_e32 v29, v69
	v_accvgpr_read_b32 v107, a37
	v_pk_fma_f32 v[60:61], v[62:63], v[24:25], v[60:61]
	v_pk_mul_f32 v[62:63], v[28:29], v[12:13]
	v_accvgpr_read_b32 v106, a36
	v_mov_b32_dpp v7, v68 row_shl:1 row_mask:0xf bank_mask:0xf
	v_pk_fma_f32 v[62:63], v[68:69], v[106:107], v[62:63] op_sel_hi:[0,1,1]
	v_mov_b32_e32 v68, v69
	v_mov_b32_e32 v69, v17
	v_mov_b32_e32 v78, v21
	v_pk_fma_f32 v[62:63], v[68:69], v[6:7], v[62:63]
	v_pk_add_f32 v[60:61], v[60:61], 0 op_sel_hi:[1,0]
	v_mov_b32_dpp v78, v83 row_shr:1 row_mask:0xf bank_mask:0xf
	v_mov_b32_e32 v53, v83
	v_accvgpr_read_b32 v14, a24
	v_pk_add_f32 v[60:61], v[60:61], v[62:63]
	v_pk_mul_f32 v[62:63], v[52:53], v[78:79]
	v_accvgpr_read_b32 v15, a25
	v_mov_b32_dpp v21, v82 row_shl:1 row_mask:0xf bank_mask:0xf
	v_pk_fma_f32 v[62:63], v[82:83], v[14:15], v[62:63] op_sel_hi:[0,1,1]
	v_mov_b32_e32 v68, v83
	v_mov_b32_e32 v69, v89
	v_pk_fma_f32 v[62:63], v[68:69], v[20:21], v[62:63]
	v_mov_b32_e32 v76, v11
	v_pk_add_f32 v[60:61], v[60:61], v[62:63]
	s_mov_b64 s[0:1], 0x410000
	v_mov_b32_dpp v76, v81 row_shr:1 row_mask:0xf bank_mask:0xf
	v_mov_b32_e32 v41, v81
	v_lshl_add_u64 v[136:137], v[134:135], 0, s[0:1]
	s_nop 1
	s_mov_b64 vcc, s[28:29]
	s_nop 0
	v_cndmask_b32_dpp v130, v60, v128, vcc quad_perm:[1,0,3,2] row_mask:0xf bank_mask:0xf
	v_cndmask_b32_dpp v131, v61, v129, vcc quad_perm:[1,0,3,2] row_mask:0xf bank_mask:0xf
	s_mov_b64 vcc, s[30:31]
	s_nop 0
	v_cndmask_b32_dpp v132, v128, v60, vcc quad_perm:[1,0,3,2] row_mask:0xf bank_mask:0xf
	v_cndmask_b32_dpp v133, v129, v61, vcc quad_perm:[1,0,3,2] row_mask:0xf bank_mask:0xf
	global_store_dwordx4 v[136:137], v[130:133], off sc0 sc1 nt
	s_nop 1
	v_pk_mul_f32 v[60:61], v[40:41], v[76:77]
	v_accvgpr_write_b32 a36, v66
	v_pk_fma_f32 v[60:61], v[80:81], v[66:67], v[60:61] op_sel_hi:[0,1,1]
	v_accvgpr_write_b32 a37, v67
	v_accvgpr_read_b32 v67, a29
	v_accvgpr_write_b32 a5, v2
	v_accvgpr_write_b32 a38, v100
	v_accvgpr_read_b32 v66, a28
	v_mov_b32_e32 v2, v35
	v_accvgpr_write_b32 a39, v101
	v_mov_b32_dpp v11, v80 row_shl:1 row_mask:0xf bank_mask:0xf
	v_pk_mov_b32 v[62:63], v[80:81], v[66:67] op_sel:[1,0]
	v_mov_b32_dpp v2, v85 row_shr:1 row_mask:0xf bank_mask:0xf
	v_mov_b32_e32 v23, v85
	v_accvgpr_read_b32 v101, a33
	v_pk_fma_f32 v[60:61], v[62:63], v[10:11], v[60:61]
	v_pk_mul_f32 v[62:63], v[22:23], v[2:3]
	v_accvgpr_read_b32 v100, a32
	v_mov_b32_dpp v35, v84 row_shl:1 row_mask:0xf bank_mask:0xf
	v_pk_fma_f32 v[62:63], v[84:85], v[100:101], v[62:63] op_sel_hi:[0,1,1]
	v_pk_mov_b32 v[68:69], v[84:85], v[8:9] op_sel:[1,0]
	v_mov_b32_e32 v92, v59
	v_pk_fma_f32 v[62:63], v[68:69], v[34:35], v[62:63]
	v_pk_add_f32 v[60:61], v[60:61], 0 op_sel_hi:[1,0]
	v_mov_b32_dpp v92, v127 row_shr:1 row_mask:0xf bank_mask:0xf
	v_mov_b32_e32 v97, v127
	v_accvgpr_read_b32 v17, a9
	v_accvgpr_read_b32 v71, a49
	v_pk_add_f32 v[60:61], v[60:61], v[62:63]
	v_pk_mul_f32 v[62:63], v[96:97], v[92:93]
	v_accvgpr_read_b32 v16, a8
	v_accvgpr_read_b32 v70, a48
	v_mov_b32_dpp v59, v126 row_shl:1 row_mask:0xf bank_mask:0xf
	v_pk_fma_f32 v[62:63], v[126:127], v[16:17], v[62:63] op_sel_hi:[0,1,1]
	v_pk_mov_b32 v[68:69], v[126:127], v[70:71] op_sel:[1,0]
	v_mov_b32_e32 v94, v57
	v_pk_fma_f32 v[62:63], v[68:69], v[58:59], v[62:63]
	v_accvgpr_write_b32 a20, v28
	v_pk_add_f32 v[60:61], v[60:61], v[62:63]
	s_mov_b64 s[0:1], 0x420000
	v_mov_b32_dpp v94, v125 row_shr:1 row_mask:0xf bank_mask:0xf
	v_mov_b32_e32 v99, v125
	v_accvgpr_read_b32 v29, a3
	v_lshl_add_u64 v[62:63], v[54:55], 0, s[0:1]
	v_mov_b32_e32 v128, v60
	v_mov_b32_e32 v129, v61
	v_pk_mul_f32 v[60:61], v[98:99], v[94:95]
	v_accvgpr_read_b32 v28, a2
	v_mov_b32_e32 v102, v51
	v_mov_b32_dpp v57, v124 row_shl:1 row_mask:0xf bank_mask:0xf
	v_pk_fma_f32 v[60:61], v[124:125], v[28:29], v[60:61] op_sel_hi:[0,1,1]
	v_mov_b32_e32 v62, v125
	v_mov_b32_e32 v63, v67
	v_mov_b32_dpp v102, v123 row_shr:1 row_mask:0xf bank_mask:0xf
	v_mov_b32_e32 v105, v123
	v_pk_fma_f32 v[60:61], v[62:63], v[56:57], v[60:61]
	v_pk_mul_f32 v[62:63], v[104:105], v[102:103]
	v_mov_b32_dpp v51, v122 row_shl:1 row_mask:0xf bank_mask:0xf
	v_pk_fma_f32 v[62:63], v[122:123], v[30:31], v[62:63] op_sel_hi:[0,1,1]
	v_accvgpr_write_b32 a28, v30
	v_mov_b32_e32 v68, v123
	v_mov_b32_e32 v69, v9
	v_mov_b32_e32 v108, v49
	v_accvgpr_write_b32 a29, v31
	v_pk_fma_f32 v[62:63], v[68:69], v[50:51], v[62:63]
	v_pk_add_f32 v[60:61], v[60:61], 0 op_sel_hi:[1,0]
	v_mov_b32_dpp v108, v121 row_shr:1 row_mask:0xf bank_mask:0xf
	v_mov_b32_e32 v111, v121
	v_accvgpr_read_b32 v31, a7
	v_pk_add_f32 v[60:61], v[60:61], v[62:63]
	v_pk_mul_f32 v[62:63], v[110:111], v[108:109]
	v_accvgpr_read_b32 v30, a6
	v_mov_b32_dpp v49, v120 row_shl:1 row_mask:0xf bank_mask:0xf
	v_pk_fma_f32 v[62:63], v[120:121], v[30:31], v[62:63] op_sel_hi:[0,1,1]
	v_mov_b32_e32 v68, v121
	v_mov_b32_e32 v69, v71
	v_pk_fma_f32 v[62:63], v[68:69], v[48:49], v[62:63]
	s_mov_b64 s[0:1], 0x430000
	v_pk_add_f32 v[60:61], v[60:61], v[62:63]
	v_lshl_add_u64 v[136:137], v[134:135], 0, s[0:1]
	v_add_u32_e32 v1, s16, v118
	s_add_u32 s0, s10, 0x1800000
	v_accvgpr_write_b32 a26, v114
	s_nop 1
	s_mov_b64 vcc, s[28:29]
	s_nop 0
	v_cndmask_b32_dpp v130, v60, v128, vcc quad_perm:[1,0,3,2] row_mask:0xf bank_mask:0xf
	v_cndmask_b32_dpp v131, v61, v129, vcc quad_perm:[1,0,3,2] row_mask:0xf bank_mask:0xf
	s_mov_b64 vcc, s[30:31]
	s_nop 0
	v_cndmask_b32_dpp v132, v128, v60, vcc quad_perm:[1,0,3,2] row_mask:0xf bank_mask:0xf
	v_cndmask_b32_dpp v133, v129, v61, vcc quad_perm:[1,0,3,2] row_mask:0xf bank_mask:0xf
	global_store_dwordx4 v[136:137], v[130:133], off sc0 sc1 nt
	s_nop 1
	v_readfirstlane_b32 s2, v1
	s_addc_u32 s1, s11, 0
	v_add_u32_e32 v1, s16, v90
	v_accvgpr_write_b32 a18, v116
	v_accvgpr_write_b32 a27, v115
	s_waitcnt vmcnt(16)
	v_lshl_add_u64 v[60:61], s[0:1], 0, v[32:33]
	s_mov_b32 m0, s2
	v_readfirstlane_b32 s2, v1
	v_add_u32_e32 v1, s16, v91
	v_accvgpr_read_b32 v115, a23
	v_accvgpr_write_b32 a19, v117
	s_waitcnt lgkmcnt(0)
	s_barrier
	global_load_lds_dwordx4 v[60:61], off nt
	v_lshl_add_u64 v[60:61], s[0:1], 0, v[74:75]
	s_mov_b32 m0, s2
	v_readfirstlane_b32 s2, v1
	v_accvgpr_read_b32 v114, a22
	v_add_u32_e32 v1, s16, v119
	v_accvgpr_read_b32 v117, a31
	global_load_lds_dwordx4 v[60:61], off nt
	v_lshl_add_u64 v[60:61], s[0:1], 0, v[114:115]
	s_mov_b32 m0, s2
	v_readfirstlane_b32 s2, v1
	v_accvgpr_read_b32 v116, a30
	global_load_lds_dwordx4 v[60:61], off nt
	v_lshl_add_u64 v[60:61], s[0:1], 0, v[116:117]
	s_mov_b32 m0, s2
	v_accvgpr_write_b32 a1, v5
	global_load_lds_dwordx4 v[60:61], off nt
	v_accvgpr_read_b32 v5, a10
	v_add_u32_e32 v2, 16, v5
	ds_read_b64 v[60:61], v2
	ds_read_b64 v[62:63], v2 offset:288
	ds_read_b64 v[68:69], v2 offset:576
	ds_read_b64 v[70:71], v2 offset:1728
	ds_read_b64 v[72:73], v2 offset:2016
	ds_read_b64 v[82:83], v2 offset:2304
	ds_read_b64 v[80:81], v2 offset:3456
	ds_read_b64 v[84:85], v2 offset:3744
	ds_read_b64 v[124:125], v2 offset:4032
	ds_read_b64 v[122:123], v2 offset:5184
	ds_read_b64 v[120:121], v2 offset:5472
	ds_read_b64 v[90:91], v2 offset:5760
	ds_read_b32 v43, v4
	ds_read_b32 v19, v4 offset:288
	ds_read_b32 v39, v4 offset:576
	ds_read_b32 v25, v4 offset:1728
	ds_read_b32 v7, v4 offset:2016
	ds_read_b32 v21, v4 offset:2304
	ds_read_b32 v11, v4 offset:3456
	ds_read_b32 v35, v4 offset:3744
	ds_read_b32 v59, v4 offset:4032
	ds_read_b32 v57, v4 offset:5184
	ds_read_b32 v51, v4 offset:5472
	ds_read_b32 v49, v4 offset:5760
	s_waitcnt lgkmcnt(0)
	v_accvgpr_write_b32 a46, v88
	v_mov_b32_e32 v46, v43
	v_accvgpr_write_b32 a8, v8
	v_mov_b32_e32 v113, v61
	v_mov_b32_dpp v46, v61 row_shr:1 row_mask:0xf bank_mask:0xf
	v_accvgpr_mov_b32 a42, a52
	v_accvgpr_write_b32 a47, v89
	v_accvgpr_write_b32 a9, v9
	v_pk_mul_f32 v[88:89], v[112:113], v[46:47]
	v_accvgpr_write_b32 a40, v112
	v_accvgpr_read_b32 v8, a18
	v_accvgpr_read_b32 v113, a39
	v_accvgpr_mov_b32 a43, a53
	v_accvgpr_write_b32 a51, v33
	v_accvgpr_write_b32 a52, v74
	v_accvgpr_read_b32 v9, a19
	v_accvgpr_read_b32 v112, a38
	v_mov_b32_e32 v26, v19
	v_accvgpr_write_b32 a50, v32
	v_accvgpr_write_b32 a53, v75
	v_mov_b32_dpp v43, v60 row_shl:1 row_mask:0xf bank_mask:0xf
	v_pk_fma_f32 v[88:89], v[60:61], v[8:9], v[88:89] op_sel_hi:[0,1,1]
	v_pk_mov_b32 v[60:61], v[60:61], v[112:113] op_sel:[1,0]
	v_mov_b32_dpp v26, v63 row_shr:1 row_mask:0xf bank_mask:0xf
	v_accvgpr_read_b32 v32, a34
	v_mov_b32_e32 v33, v63
	v_accvgpr_read_b32 v127, a27
	v_accvgpr_read_b32 v75, a43
	v_pk_fma_f32 v[60:61], v[60:61], v[42:43], v[88:89]
	v_pk_mul_f32 v[88:89], v[32:33], v[26:27]
	v_accvgpr_read_b32 v126, a26
	v_accvgpr_read_b32 v74, a42
	v_mov_b32_dpp v19, v62 row_shl:1 row_mask:0xf bank_mask:0xf
	v_pk_fma_f32 v[88:89], v[62:63], v[126:127], v[88:89] op_sel_hi:[0,1,1]
	v_pk_mov_b32 v[62:63], v[62:63], v[74:75] op_sel:[1,0]
	v_mov_b32_e32 v44, v39
	v_accvgpr_mov_b32 a14, a48
	v_pk_fma_f32 v[62:63], v[62:63], v[18:19], v[88:89]
	v_pk_add_f32 v[60:61], v[60:61], 0 op_sel_hi:[1,0]
	v_mov_b32_dpp v44, v69 row_shr:1 row_mask:0xf bank_mask:0xf
	v_mov_b32_e32 v1, v69
	v_accvgpr_mov_b32 a15, a49
	v_pk_add_f32 v[60:61], v[60:61], v[62:63]
	v_pk_mul_f32 v[62:63], v[0:1], v[44:45]
	v_accvgpr_write_b32 a48, v0
	v_accvgpr_read_b32 v89, a45
	v_accvgpr_read_b32 v0, a46
	v_accvgpr_read_b32 v88, a44
	v_accvgpr_read_b32 v1, a47
	v_mov_b32_dpp v39, v68 row_shl:1 row_mask:0xf bank_mask:0xf
	v_pk_fma_f32 v[62:63], v[68:69], v[88:89], v[62:63] op_sel_hi:[0,1,1]
	v_pk_mov_b32 v[68:69], v[68:69], v[0:1] op_sel:[1,0]
	v_mov_b32_e32 v36, v25
	v_pk_fma_f32 v[62:63], v[68:69], v[38:39], v[62:63]
	s_mov_b64 s[0:1], 0x800000
	v_pk_add_f32 v[60:61], v[60:61], v[62:63]
	v_mov_b32_dpp v36, v71 row_shr:1 row_mask:0xf bank_mask:0xf
	v_mov_b32_e32 v65, v71
	v_lshl_add_u64 v[62:63], v[54:55], 0, s[0:1]
	v_mov_b32_e32 v128, v60
	v_mov_b32_e32 v129, v61
	v_pk_mul_f32 v[60:61], v[64:65], v[36:37]
	v_mov_b64_e32 v[118:119], v[86:87]
	v_mov_b32_e32 v12, v7
	v_accvgpr_write_b32 a24, v32
	v_mov_b32_dpp v25, v70 row_shl:1 row_mask:0xf bank_mask:0xf
	v_pk_fma_f32 v[60:61], v[70:71], v[118:119], v[60:61] op_sel_hi:[0,1,1]
	v_mov_b32_e32 v62, v71
	v_mov_b32_e32 v63, v113
	v_mov_b32_dpp v12, v73 row_shr:1 row_mask:0xf bank_mask:0xf
	v_accvgpr_read_b32 v32, a20
	v_mov_b32_e32 v33, v73
	v_pk_fma_f32 v[60:61], v[62:63], v[24:25], v[60:61]
	v_pk_mul_f32 v[62:63], v[32:33], v[12:13]
	v_mov_b32_dpp v7, v72 row_shl:1 row_mask:0xf bank_mask:0xf
	v_pk_fma_f32 v[62:63], v[72:73], v[106:107], v[62:63] op_sel_hi:[0,1,1]
	v_mov_b32_e32 v68, v73
	v_mov_b32_e32 v69, v75
	v_mov_b32_e32 v78, v21
	v_pk_fma_f32 v[62:63], v[68:69], v[6:7], v[62:63]
	v_pk_add_f32 v[60:61], v[60:61], 0 op_sel_hi:[1,0]
	v_mov_b32_dpp v78, v83 row_shr:1 row_mask:0xf bank_mask:0xf
	v_mov_b32_e32 v53, v83
	v_pk_add_f32 v[60:61], v[60:61], v[62:63]
	v_pk_mul_f32 v[62:63], v[52:53], v[78:79]
	v_mov_b32_dpp v21, v82 row_shl:1 row_mask:0xf bank_mask:0xf
	v_pk_fma_f32 v[62:63], v[82:83], v[14:15], v[62:63] op_sel_hi:[0,1,1]
	v_mov_b32_e32 v68, v83
	v_mov_b32_e32 v69, v1
	v_accvgpr_write_b32 a19, v15
	v_pk_fma_f32 v[62:63], v[68:69], v[20:21], v[62:63]
	v_mov_b32_e32 v76, v11
	v_accvgpr_write_b32 a18, v14
	v_pk_add_f32 v[60:61], v[60:61], v[62:63]
	s_mov_b64 s[0:1], 0x810000
	v_mov_b32_dpp v76, v81 row_shr:1 row_mask:0xf bank_mask:0xf
	v_mov_b32_e32 v41, v81
	v_accvgpr_read_b32 v14, a36
	v_accvgpr_write_b32 a6, v2
	v_lshl_add_u64 v[136:137], v[134:135], 0, s[0:1]
	s_nop 1
	s_mov_b64 vcc, s[28:29]
	s_nop 0
	v_cndmask_b32_dpp v130, v60, v128, vcc quad_perm:[1,0,3,2] row_mask:0xf bank_mask:0xf
	v_cndmask_b32_dpp v131, v61, v129, vcc quad_perm:[1,0,3,2] row_mask:0xf bank_mask:0xf
	s_mov_b64 vcc, s[30:31]
	s_nop 0
	v_cndmask_b32_dpp v132, v128, v60, vcc quad_perm:[1,0,3,2] row_mask:0xf bank_mask:0xf
	v_cndmask_b32_dpp v133, v129, v61, vcc quad_perm:[1,0,3,2] row_mask:0xf bank_mask:0xf
	global_store_dwordx4 v[136:137], v[130:133], off sc0 sc1 nt
	s_nop 1
	v_pk_mul_f32 v[60:61], v[40:41], v[76:77]
	v_accvgpr_read_b32 v15, a37
	v_mov_b32_e32 v2, v35
	v_mov_b32_dpp v11, v80 row_shl:1 row_mask:0xf bank_mask:0xf
	v_pk_fma_f32 v[60:61], v[80:81], v[14:15], v[60:61] op_sel_hi:[0,1,1]
	v_pk_mov_b32 v[62:63], v[80:81], v[66:67] op_sel:[1,0]
	v_mov_b32_dpp v2, v85 row_shr:1 row_mask:0xf bank_mask:0xf
	v_mov_b32_e32 v23, v85
	v_accvgpr_read_b32 v15, a9
	v_pk_fma_f32 v[60:61], v[62:63], v[10:11], v[60:61]
	v_pk_mul_f32 v[62:63], v[22:23], v[2:3]
	v_accvgpr_read_b32 v14, a8
	v_mov_b32_dpp v35, v84 row_shl:1 row_mask:0xf bank_mask:0xf
	v_pk_fma_f32 v[62:63], v[84:85], v[100:101], v[62:63] op_sel_hi:[0,1,1]
	v_pk_mov_b32 v[68:69], v[84:85], v[14:15] op_sel:[1,0]
	v_mov_b32_e32 v92, v59
	v_pk_fma_f32 v[62:63], v[68:69], v[34:35], v[62:63]
	v_pk_add_f32 v[60:61], v[60:61], 0 op_sel_hi:[1,0]
	v_mov_b32_dpp v92, v125 row_shr:1 row_mask:0xf bank_mask:0xf
	v_mov_b32_e32 v97, v125
	v_accvgpr_read_b32 v71, a15
	v_pk_add_f32 v[60:61], v[60:61], v[62:63]
	v_pk_mul_f32 v[62:63], v[96:97], v[92:93]
	v_accvgpr_read_b32 v70, a14
	v_mov_b32_dpp v59, v124 row_shl:1 row_mask:0xf bank_mask:0xf
	v_pk_fma_f32 v[62:63], v[124:125], v[16:17], v[62:63] op_sel_hi:[0,1,1]
	v_pk_mov_b32 v[68:69], v[124:125], v[70:71] op_sel:[1,0]
	v_mov_b32_e32 v94, v57
	v_pk_fma_f32 v[62:63], v[68:69], v[58:59], v[62:63]
	s_mov_b64 s[0:1], 0x820000
	v_pk_add_f32 v[60:61], v[60:61], v[62:63]
	v_mov_b32_dpp v94, v123 row_shr:1 row_mask:0xf bank_mask:0xf
	v_mov_b32_e32 v99, v123
	v_accvgpr_write_b32 a31, v17
	v_lshl_add_u64 v[62:63], v[54:55], 0, s[0:1]
	v_mov_b32_e32 v128, v60
	v_mov_b32_e32 v129, v61
	v_pk_mul_f32 v[60:61], v[98:99], v[94:95]
	v_mov_b32_e32 v102, v51
	v_accvgpr_write_b32 a30, v16
	v_mov_b32_dpp v57, v122 row_shl:1 row_mask:0xf bank_mask:0xf
	v_pk_fma_f32 v[60:61], v[122:123], v[28:29], v[60:61] op_sel_hi:[0,1,1]
	v_mov_b32_e32 v62, v123
	v_mov_b32_e32 v63, v67
	v_mov_b32_dpp v102, v121 row_shr:1 row_mask:0xf bank_mask:0xf
	v_mov_b32_e32 v105, v121
	v_accvgpr_read_b32 v16, a28
	v_pk_fma_f32 v[60:61], v[62:63], v[56:57], v[60:61]
	v_pk_mul_f32 v[62:63], v[104:105], v[102:103]
	v_accvgpr_read_b32 v17, a29
	v_mov_b32_dpp v51, v120 row_shl:1 row_mask:0xf bank_mask:0xf
	v_pk_fma_f32 v[62:63], v[120:121], v[16:17], v[62:63] op_sel_hi:[0,1,1]
	v_mov_b32_e32 v68, v121
	v_mov_b32_e32 v69, v15
	v_mov_b32_e32 v108, v49
	v_pk_fma_f32 v[62:63], v[68:69], v[50:51], v[62:63]
	v_pk_add_f32 v[60:61], v[60:61], 0 op_sel_hi:[1,0]
	v_mov_b32_dpp v108, v91 row_shr:1 row_mask:0xf bank_mask:0xf
	v_mov_b32_e32 v111, v91
	v_pk_add_f32 v[60:61], v[60:61], v[62:63]
	v_pk_mul_f32 v[62:63], v[110:111], v[108:109]
	v_mov_b32_dpp v49, v90 row_shl:1 row_mask:0xf bank_mask:0xf
	v_pk_fma_f32 v[62:63], v[90:91], v[30:31], v[62:63] op_sel_hi:[0,1,1]
	v_mov_b32_e32 v68, v91
	v_mov_b32_e32 v69, v71
	v_pk_fma_f32 v[62:63], v[68:69], v[48:49], v[62:63]
	s_mov_b64 s[0:1], 0x830000
	v_mov_b32_e32 v0, v22
	v_pk_add_f32 v[60:61], v[60:61], v[62:63]
	v_lshl_add_u64 v[136:137], v[134:135], 0, s[0:1]
	s_add_u32 s0, s10, 0x1c00000
	v_accvgpr_read_b32 v22, a50
	v_accvgpr_read_b32 v1, a72
	s_addc_u32 s1, s11, 0
	v_accvgpr_read_b32 v23, a51
	s_nop 1
	s_mov_b64 vcc, s[28:29]
	s_nop 0
	v_cndmask_b32_dpp v130, v60, v128, vcc quad_perm:[1,0,3,2] row_mask:0xf bank_mask:0xf
	v_cndmask_b32_dpp v131, v61, v129, vcc quad_perm:[1,0,3,2] row_mask:0xf bank_mask:0xf
	s_mov_b64 vcc, s[30:31]
	s_nop 0
	v_cndmask_b32_dpp v132, v128, v60, vcc quad_perm:[1,0,3,2] row_mask:0xf bank_mask:0xf
	v_cndmask_b32_dpp v133, v129, v61, vcc quad_perm:[1,0,3,2] row_mask:0xf bank_mask:0xf
	global_store_dwordx4 v[136:137], v[130:133], off sc0 sc1 nt
	s_nop 1
	v_readfirstlane_b32 s2, v1
	v_lshl_add_u64 v[60:61], s[0:1], 0, v[22:23]
	v_accvgpr_read_b32 v1, a12
	v_accvgpr_read_b32 v22, a52
	s_waitcnt vmcnt(18)
	s_mov_b32 m0, s2
	v_readfirstlane_b32 s2, v1
	v_accvgpr_read_b32 v23, a53
	v_accvgpr_read_b32 v1, a13
	s_waitcnt lgkmcnt(0)
	s_barrier
	global_load_lds_dwordx4 v[60:61], off nt
	v_lshl_add_u64 v[60:61], s[0:1], 0, v[22:23]
	s_mov_b32 m0, s2
	v_readfirstlane_b32 s2, v1
	v_accvgpr_read_b32 v1, a16
	global_load_lds_dwordx4 v[60:61], off nt
	v_lshl_add_u64 v[60:61], s[0:1], 0, v[114:115]
	s_mov_b32 m0, s2
	v_readfirstlane_b32 s2, v1
	global_load_lds_dwordx4 v[60:61], off nt
	v_lshl_add_u64 v[60:61], s[0:1], 0, v[116:117]
	s_mov_b32 m0, s2
	v_accvgpr_write_b32 a22, v30
	v_accvgpr_write_b32 a44, v70
	global_load_lds_dwordx4 v[60:61], off nt
	v_accvgpr_write_b32 a2, v106
	v_accvgpr_write_b32 a34, v74
	v_accvgpr_write_b32 a23, v31
	v_accvgpr_write_b32 a45, v71
	v_add_u32_e32 v2, 0x7010, v5
	v_mov_b32_e32 v31, v5
	v_add_u32_e32 v5, 0x7000, v4
	ds_read_b64 v[60:61], v2
	ds_read_b64 v[62:63], v2 offset:288
	ds_read_b64 v[68:69], v2 offset:576
	ds_read_b64 v[70:71], v2 offset:1728
	ds_read_b64 v[72:73], v2 offset:2016
	ds_read_b64 v[82:83], v2 offset:2304
	ds_read_b64 v[80:81], v2 offset:3456
	ds_read_b64 v[84:85], v2 offset:3744
	ds_read_b64 v[116:117], v2 offset:4032
	ds_read_b64 v[114:115], v2 offset:5184
	ds_read_b64 v[112:113], v2 offset:5472
	ds_read_b64 v[90:91], v2 offset:5760
	ds_read_b32 v43, v5
	ds_read_b32 v19, v5 offset:288
	ds_read_b32 v39, v5 offset:576
	ds_read_b32 v25, v5 offset:1728
	ds_read_b32 v7, v5 offset:2016
	ds_read_b32 v21, v5 offset:2304
	ds_read_b32 v11, v5 offset:3456
	ds_read_b32 v35, v5 offset:3744
	ds_read_b32 v59, v5 offset:4032
	ds_read_b32 v57, v5 offset:5184
	ds_read_b32 v51, v5 offset:5472
	ds_read_b32 v49, v5 offset:5760
	s_waitcnt lgkmcnt(0)
	v_accvgpr_write_b32 a3, v107
	v_mov_b32_e32 v46, v43
	v_accvgpr_write_b32 a35, v75
	v_accvgpr_read_b32 v74, a40
	v_mov_b32_dpp v46, v61 row_shr:1 row_mask:0xf bank_mask:0xf
	v_mov_b32_e32 v75, v61
	v_accvgpr_read_b32 v107, a39
	v_accvgpr_write_b32 a10, v100
	v_pk_mul_f32 v[86:87], v[74:75], v[46:47]
	v_accvgpr_read_b32 v106, a38
	v_mov_b32_e32 v26, v19
	v_accvgpr_write_b32 a11, v101
	v_mov_b32_dpp v43, v60 row_shl:1 row_mask:0xf bank_mask:0xf
	v_mov_b32_e32 v32, v74
	v_pk_fma_f32 v[86:87], v[60:61], v[8:9], v[86:87] op_sel_hi:[0,1,1]
	v_pk_mov_b32 v[60:61], v[60:61], v[106:107] op_sel:[1,0]
	v_mov_b32_dpp v26, v63 row_shr:1 row_mask:0xf bank_mask:0xf
	v_accvgpr_read_b32 v74, a24
	v_mov_b32_e32 v75, v63
	v_accvgpr_read_b32 v101, a35
	v_pk_fma_f32 v[60:61], v[60:61], v[42:43], v[86:87]
	v_pk_mul_f32 v[86:87], v[74:75], v[26:27]
	v_accvgpr_read_b32 v100, a34
	v_accvgpr_write_b32 a14, v66
	v_mov_b32_dpp v19, v62 row_shl:1 row_mask:0xf bank_mask:0xf
	v_pk_fma_f32 v[86:87], v[62:63], v[126:127], v[86:87] op_sel_hi:[0,1,1]
	v_pk_mov_b32 v[62:63], v[62:63], v[100:101] op_sel:[1,0]
	v_mov_b32_e32 v44, v39
	v_accvgpr_write_b32 a42, v64
	v_accvgpr_write_b32 a15, v67
	v_mov_b32_e32 v66, v4
	v_pk_fma_f32 v[62:63], v[62:63], v[18:19], v[86:87]
	v_pk_add_f32 v[60:61], v[60:61], 0 op_sel_hi:[1,0]
	v_mov_b32_dpp v44, v69 row_shr:1 row_mask:0xf bank_mask:0xf
	v_accvgpr_read_b32 v64, a48
	v_mov_b32_e32 v65, v69
	v_accvgpr_read_b32 v4, a46
	v_pk_add_f32 v[60:61], v[60:61], v[62:63]
	v_pk_mul_f32 v[62:63], v[64:65], v[44:45]
	v_accvgpr_read_b32 v5, a47
	v_mov_b32_dpp v39, v68 row_shl:1 row_mask:0xf bank_mask:0xf
	v_pk_fma_f32 v[62:63], v[68:69], v[88:89], v[62:63] op_sel_hi:[0,1,1]
	v_pk_mov_b32 v[68:69], v[68:69], v[4:5] op_sel:[1,0]
	v_mov_b32_e32 v36, v25
	v_pk_fma_f32 v[62:63], v[68:69], v[38:39], v[62:63]
	s_mov_b64 s[0:1], 0xc00000
	v_pk_add_f32 v[60:61], v[60:61], v[62:63]
	v_mov_b32_dpp v36, v71 row_shr:1 row_mask:0xf bank_mask:0xf
	v_accvgpr_read_b32 v22, a42
	v_mov_b32_e32 v23, v71
	v_accvgpr_mov_b32 a26, a20
	v_accvgpr_write_b32 a20, v28
	v_lshl_add_u64 v[62:63], v[54:55], 0, s[0:1]
	v_mov_b32_e32 v128, v60
	v_mov_b32_e32 v129, v61
	v_pk_mul_f32 v[60:61], v[22:23], v[36:37]
	v_mov_b32_e32 v12, v7
	v_accvgpr_write_b32 a21, v29
	v_mov_b32_dpp v25, v70 row_shl:1 row_mask:0xf bank_mask:0xf
	v_pk_fma_f32 v[60:61], v[70:71], v[118:119], v[60:61] op_sel_hi:[0,1,1]
	v_mov_b32_e32 v62, v71
	v_mov_b32_e32 v63, v107
	v_mov_b32_dpp v12, v73 row_shr:1 row_mask:0xf bank_mask:0xf
	v_accvgpr_read_b32 v28, a26
	v_mov_b32_e32 v29, v73
	v_accvgpr_read_b32 v121, a3
	v_pk_fma_f32 v[60:61], v[62:63], v[24:25], v[60:61]
	v_pk_mul_f32 v[62:63], v[28:29], v[12:13]
	v_accvgpr_read_b32 v120, a2
	v_mov_b32_dpp v7, v72 row_shl:1 row_mask:0xf bank_mask:0xf
	v_pk_fma_f32 v[62:63], v[72:73], v[120:121], v[62:63] op_sel_hi:[0,1,1]
	v_mov_b32_e32 v68, v73
	v_mov_b32_e32 v69, v101
	v_mov_b32_e32 v78, v21
	v_pk_fma_f32 v[62:63], v[68:69], v[6:7], v[62:63]
	v_pk_add_f32 v[60:61], v[60:61], 0 op_sel_hi:[1,0]
	v_mov_b32_dpp v78, v83 row_shr:1 row_mask:0xf bank_mask:0xf
	v_mov_b32_e32 v53, v83
	v_accvgpr_read_b32 v125, a19
	v_pk_add_f32 v[60:61], v[60:61], v[62:63]
	v_pk_mul_f32 v[62:63], v[52:53], v[78:79]
	v_accvgpr_read_b32 v124, a18
	v_mov_b32_dpp v21, v82 row_shl:1 row_mask:0xf bank_mask:0xf
	v_pk_fma_f32 v[62:63], v[82:83], v[124:125], v[62:63] op_sel_hi:[0,1,1]
	v_mov_b32_e32 v68, v83
	v_mov_b32_e32 v69, v5
	v_pk_fma_f32 v[62:63], v[68:69], v[20:21], v[62:63]
	v_mov_b32_e32 v76, v11
	v_pk_add_f32 v[60:61], v[60:61], v[62:63]
	s_mov_b64 s[0:1], 0xc10000
	v_mov_b32_dpp v76, v81 row_shr:1 row_mask:0xf bank_mask:0xf
	v_mov_b32_e32 v41, v81
	v_accvgpr_read_b32 v123, a37
	v_accvgpr_read_b32 v4, a14
	v_lshl_add_u64 v[136:137], v[134:135], 0, s[0:1]
	s_nop 1
	s_mov_b64 vcc, s[28:29]
	s_nop 0
	v_cndmask_b32_dpp v130, v60, v128, vcc quad_perm:[1,0,3,2] row_mask:0xf bank_mask:0xf
	v_cndmask_b32_dpp v131, v61, v129, vcc quad_perm:[1,0,3,2] row_mask:0xf bank_mask:0xf
	s_mov_b64 vcc, s[30:31]
	s_nop 0
	v_cndmask_b32_dpp v132, v128, v60, vcc quad_perm:[1,0,3,2] row_mask:0xf bank_mask:0xf
	v_cndmask_b32_dpp v133, v129, v61, vcc quad_perm:[1,0,3,2] row_mask:0xf bank_mask:0xf
	global_store_dwordx4 v[136:137], v[130:133], off sc0 sc1 nt
	s_nop 1
	v_pk_mul_f32 v[60:61], v[40:41], v[76:77]
	v_accvgpr_read_b32 v122, a36
	v_accvgpr_read_b32 v5, a15
	v_mov_b32_e32 v2, v35
	v_accvgpr_mov_b32 a32, a24
	v_accvgpr_write_b32 a24, v22
	v_mov_b64_e32 v[22:23], v[118:119]
	v_mov_b32_dpp v11, v80 row_shl:1 row_mask:0xf bank_mask:0xf
	v_pk_fma_f32 v[60:61], v[80:81], v[122:123], v[60:61] op_sel_hi:[0,1,1]
	v_pk_mov_b32 v[62:63], v[80:81], v[4:5] op_sel:[1,0]
	v_mov_b32_dpp v2, v85 row_shr:1 row_mask:0xf bank_mask:0xf
	v_mov_b32_e32 v106, v0
	v_mov_b32_e32 v107, v85
	v_accvgpr_read_b32 v119, a11
	v_pk_fma_f32 v[60:61], v[62:63], v[10:11], v[60:61]
	v_pk_mul_f32 v[62:63], v[106:107], v[2:3]
	v_accvgpr_read_b32 v118, a10
	v_mov_b64_e32 v[100:101], v[14:15]
	v_mov_b32_dpp v35, v84 row_shl:1 row_mask:0xf bank_mask:0xf
	v_pk_fma_f32 v[62:63], v[84:85], v[118:119], v[62:63] op_sel_hi:[0,1,1]
	v_pk_mov_b32 v[68:69], v[84:85], v[100:101] op_sel:[1,0]
	v_mov_b32_e32 v92, v59
	v_accvgpr_write_b32 a26, v52
	v_mov_b32_e32 v74, v40
	v_pk_fma_f32 v[62:63], v[68:69], v[34:35], v[62:63]
	v_pk_add_f32 v[60:61], v[60:61], 0 op_sel_hi:[1,0]
	v_mov_b32_dpp v92, v117 row_shr:1 row_mask:0xf bank_mask:0xf
	v_mov_b32_e32 v97, v117
	v_accvgpr_read_b32 v41, a31
	v_accvgpr_read_b32 v53, a45
	v_pk_add_f32 v[60:61], v[60:61], v[62:63]
	v_pk_mul_f32 v[62:63], v[96:97], v[92:93]
	v_accvgpr_read_b32 v40, a30
	v_accvgpr_read_b32 v52, a44
	v_mov_b32_dpp v59, v116 row_shl:1 row_mask:0xf bank_mask:0xf
	v_pk_fma_f32 v[62:63], v[116:117], v[40:41], v[62:63] op_sel_hi:[0,1,1]
	v_pk_mov_b32 v[68:69], v[116:117], v[52:53] op_sel:[1,0]
	v_mov_b32_e32 v94, v57
	v_pk_fma_f32 v[62:63], v[68:69], v[58:59], v[62:63]
	s_mov_b64 s[0:1], 0xc20000
	v_pk_add_f32 v[60:61], v[60:61], v[62:63]
	v_mov_b32_dpp v94, v115 row_shr:1 row_mask:0xf bank_mask:0xf
	v_mov_b32_e32 v99, v115
	v_accvgpr_read_b32 v14, a20
	v_lshl_add_u64 v[62:63], v[54:55], 0, s[0:1]
	v_mov_b32_e32 v128, v60
	v_mov_b32_e32 v129, v61
	v_pk_mul_f32 v[60:61], v[98:99], v[94:95]
	v_accvgpr_read_b32 v15, a21
	v_mov_b32_e32 v102, v51
	v_mov_b32_dpp v57, v114 row_shl:1 row_mask:0xf bank_mask:0xf
	v_pk_fma_f32 v[60:61], v[114:115], v[14:15], v[60:61] op_sel_hi:[0,1,1]
	v_mov_b32_e32 v62, v115
	v_mov_b32_e32 v63, v5
	v_mov_b32_dpp v102, v113 row_shr:1 row_mask:0xf bank_mask:0xf
	v_mov_b32_e32 v105, v113
	v_pk_fma_f32 v[60:61], v[62:63], v[56:57], v[60:61]
	v_pk_mul_f32 v[62:63], v[104:105], v[102:103]
	v_accvgpr_write_b32 a8, v8
	v_mov_b32_dpp v51, v112 row_shl:1 row_mask:0xf bank_mask:0xf
	v_pk_fma_f32 v[62:63], v[112:113], v[16:17], v[62:63] op_sel_hi:[0,1,1]
	v_mov_b32_e32 v68, v113
	v_mov_b32_e32 v69, v101
	v_mov_b32_e32 v108, v49
	v_accvgpr_write_b32 a9, v9
	v_pk_fma_f32 v[62:63], v[68:69], v[50:51], v[62:63]
	v_pk_add_f32 v[60:61], v[60:61], 0 op_sel_hi:[1,0]
	v_mov_b32_dpp v108, v91 row_shr:1 row_mask:0xf bank_mask:0xf
	v_mov_b32_e32 v111, v91
	v_accvgpr_read_b32 v8, a22
	v_pk_add_f32 v[60:61], v[60:61], v[62:63]
	v_pk_mul_f32 v[62:63], v[110:111], v[108:109]
	v_accvgpr_read_b32 v9, a23
	v_mov_b32_dpp v49, v90 row_shl:1 row_mask:0xf bank_mask:0xf
	v_pk_fma_f32 v[62:63], v[90:91], v[8:9], v[62:63] op_sel_hi:[0,1,1]
	v_mov_b32_e32 v68, v91
	v_mov_b32_e32 v69, v53
	v_pk_fma_f32 v[62:63], v[68:69], v[48:49], v[62:63]
	s_mov_b64 s[0:1], 0xc30000
	v_pk_add_f32 v[60:61], v[60:61], v[62:63]
	v_lshl_add_u64 v[136:137], v[134:135], 0, s[0:1]
	s_nop 1
	s_mov_b64 vcc, s[28:29]
	s_nop 0
	v_cndmask_b32_dpp v130, v60, v128, vcc quad_perm:[1,0,3,2] row_mask:0xf bank_mask:0xf
	v_cndmask_b32_dpp v131, v61, v129, vcc quad_perm:[1,0,3,2] row_mask:0xf bank_mask:0xf
	s_mov_b64 vcc, s[30:31]
	s_nop 0
	v_cndmask_b32_dpp v132, v128, v60, vcc quad_perm:[1,0,3,2] row_mask:0xf bank_mask:0xf
	v_cndmask_b32_dpp v133, v129, v61, vcc quad_perm:[1,0,3,2] row_mask:0xf bank_mask:0xf
	global_store_dwordx4 v[136:137], v[130:133], off sc0 sc1 nt
	s_nop 1
	s_waitcnt vmcnt(20)
	v_accvgpr_write_b32 a16, v88
	v_accvgpr_write_b32 a10, v100
	s_waitcnt lgkmcnt(0)
	s_barrier
	v_add_u32_e32 v2, 0xe010, v31
	v_add_u32_e32 v5, 0xe000, v66
	ds_read_b64 v[60:61], v2
	ds_read_b64 v[62:63], v2 offset:288
	ds_read_b64 v[68:69], v2 offset:576
	ds_read_b64 v[70:71], v2 offset:1728
	ds_read_b64 v[72:73], v2 offset:2016
	ds_read_b64 v[82:83], v2 offset:2304
	ds_read_b64 v[80:81], v2 offset:3456
	ds_read_b64 v[84:85], v2 offset:3744
	ds_read_b64 v[116:117], v2 offset:4032
	ds_read_b64 v[114:115], v2 offset:5184
	ds_read_b64 v[112:113], v2 offset:5472
	ds_read_b64 v[90:91], v2 offset:5760
	ds_read_b32 v43, v5
	ds_read_b32 v19, v5 offset:288
	ds_read_b32 v39, v5 offset:576
	ds_read_b32 v25, v5 offset:1728
	ds_read_b32 v7, v5 offset:2016
	ds_read_b32 v21, v5 offset:2304
	ds_read_b32 v11, v5 offset:3456
	ds_read_b32 v35, v5 offset:3744
	ds_read_b32 v59, v5 offset:4032
	ds_read_b32 v57, v5 offset:5184
	ds_read_b32 v51, v5 offset:5472
	ds_read_b32 v49, v5 offset:5760
	s_waitcnt lgkmcnt(0)
	v_accvgpr_write_b32 a17, v89
	v_mov_b32_e32 v46, v43
	v_accvgpr_write_b32 a11, v101
	v_mov_b32_e32 v33, v61
	v_mov_b32_dpp v46, v61 row_shr:1 row_mask:0xf bank_mask:0xf
	v_accvgpr_read_b32 v89, a9
	v_accvgpr_read_b32 v101, a39
	v_pk_mul_f32 v[86:87], v[32:33], v[46:47]
	v_accvgpr_read_b32 v88, a8
	v_accvgpr_read_b32 v100, a38
	v_mov_b32_e32 v26, v19
	v_accvgpr_write_b32 a19, v17
	v_mov_b32_dpp v43, v60 row_shl:1 row_mask:0xf bank_mask:0xf
	v_pk_fma_f32 v[86:87], v[60:61], v[88:89], v[86:87] op_sel_hi:[0,1,1]
	v_pk_mov_b32 v[60:61], v[60:61], v[100:101] op_sel:[1,0]
	v_mov_b32_dpp v26, v63 row_shr:1 row_mask:0xf bank_mask:0xf
	v_accvgpr_read_b32 v0, a32
	v_mov_b32_e32 v1, v63
	v_accvgpr_read_b32 v4, a34
	v_accvgpr_write_b32 a18, v16
	v_pk_fma_f32 v[60:61], v[60:61], v[42:43], v[86:87]
	v_pk_mul_f32 v[86:87], v[0:1], v[26:27]
	v_mov_b64_e32 v[16:17], v[126:127]
	v_accvgpr_read_b32 v5, a35
	v_mov_b32_dpp v19, v62 row_shl:1 row_mask:0xf bank_mask:0xf
	v_pk_fma_f32 v[86:87], v[62:63], v[16:17], v[86:87] op_sel_hi:[0,1,1]
	v_pk_mov_b32 v[62:63], v[62:63], v[4:5] op_sel:[1,0]
	v_mov_b32_e32 v44, v39
	v_accvgpr_read_b32 v30, a48
	v_mov_b32_e32 v64, v28
	v_accvgpr_write_b32 a7, v66
	v_pk_fma_f32 v[62:63], v[62:63], v[18:19], v[86:87]
	v_pk_add_f32 v[60:61], v[60:61], 0 op_sel_hi:[1,0]
	v_mov_b32_dpp v44, v69 row_shr:1 row_mask:0xf bank_mask:0xf
	v_mov_b32_e32 v31, v69
	v_accvgpr_read_b32 v29, a17
	v_accvgpr_read_b32 v67, a47
	v_pk_add_f32 v[60:61], v[60:61], v[62:63]
	v_pk_mul_f32 v[62:63], v[30:31], v[44:45]
	v_accvgpr_read_b32 v28, a16
	v_accvgpr_read_b32 v66, a46
	v_mov_b32_dpp v39, v68 row_shl:1 row_mask:0xf bank_mask:0xf
	v_pk_fma_f32 v[62:63], v[68:69], v[28:29], v[62:63] op_sel_hi:[0,1,1]
	v_pk_mov_b32 v[68:69], v[68:69], v[66:67] op_sel:[1,0]
	v_mov_b32_e32 v36, v25
	v_pk_fma_f32 v[62:63], v[68:69], v[38:39], v[62:63]
	s_mov_b64 s[0:1], 0x1000000
	v_pk_add_f32 v[60:61], v[60:61], v[62:63]
	v_mov_b32_dpp v36, v71 row_shr:1 row_mask:0xf bank_mask:0xf
	v_accvgpr_read_b32 v126, a24
	v_mov_b32_e32 v127, v71
	v_lshl_add_u64 v[62:63], v[54:55], 0, s[0:1]
	v_mov_b32_e32 v128, v60
	v_mov_b32_e32 v129, v61
	v_pk_mul_f32 v[60:61], v[126:127], v[36:37]
	v_mov_b32_e32 v12, v7
	v_mov_b32_dpp v25, v70 row_shl:1 row_mask:0xf bank_mask:0xf
	v_pk_fma_f32 v[60:61], v[70:71], v[22:23], v[60:61] op_sel_hi:[0,1,1]
	v_mov_b32_e32 v62, v71
	v_mov_b32_e32 v63, v101
	v_mov_b32_dpp v12, v73 row_shr:1 row_mask:0xf bank_mask:0xf
	v_mov_b32_e32 v52, v64
	v_mov_b32_e32 v53, v73
	v_pk_fma_f32 v[60:61], v[62:63], v[24:25], v[60:61]
	v_pk_mul_f32 v[62:63], v[52:53], v[12:13]
	v_mov_b32_dpp v7, v72 row_shl:1 row_mask:0xf bank_mask:0xf
	v_pk_fma_f32 v[62:63], v[72:73], v[120:121], v[62:63] op_sel_hi:[0,1,1]
	v_mov_b32_e32 v68, v73
	v_mov_b32_e32 v69, v5
	v_mov_b32_e32 v78, v21
	v_pk_fma_f32 v[62:63], v[68:69], v[6:7], v[62:63]
	v_pk_add_f32 v[60:61], v[60:61], 0 op_sel_hi:[1,0]
	v_mov_b32_dpp v78, v83 row_shr:1 row_mask:0xf bank_mask:0xf
	v_accvgpr_read_b32 v4, a26
	v_mov_b32_e32 v5, v83
	v_pk_add_f32 v[60:61], v[60:61], v[62:63]
	v_pk_mul_f32 v[62:63], v[4:5], v[78:79]
	v_mov_b32_dpp v21, v82 row_shl:1 row_mask:0xf bank_mask:0xf
	v_pk_fma_f32 v[62:63], v[82:83], v[124:125], v[62:63] op_sel_hi:[0,1,1]
	v_mov_b32_e32 v68, v83
	v_mov_b32_e32 v69, v67
	v_accvgpr_write_b32 a8, v120
	v_pk_fma_f32 v[62:63], v[68:69], v[20:21], v[62:63]
	v_mov_b32_e32 v76, v11
	v_accvgpr_write_b32 a9, v121
	v_pk_add_f32 v[60:61], v[60:61], v[62:63]
	s_mov_b64 s[0:1], 0x1010000
	v_mov_b32_dpp v76, v81 row_shr:1 row_mask:0xf bank_mask:0xf
	v_mov_b32_e32 v120, v74
	v_mov_b32_e32 v121, v81
	v_accvgpr_read_b32 v101, a15
	v_accvgpr_mov_b32 a12, a38
	v_lshl_add_u64 v[136:137], v[134:135], 0, s[0:1]
	s_nop 1
	s_mov_b64 vcc, s[28:29]
	s_nop 0
	v_cndmask_b32_dpp v130, v60, v128, vcc quad_perm:[1,0,3,2] row_mask:0xf bank_mask:0xf
	v_cndmask_b32_dpp v131, v61, v129, vcc quad_perm:[1,0,3,2] row_mask:0xf bank_mask:0xf
	s_mov_b64 vcc, s[30:31]
	s_nop 0
	v_cndmask_b32_dpp v132, v128, v60, vcc quad_perm:[1,0,3,2] row_mask:0xf bank_mask:0xf
	v_cndmask_b32_dpp v133, v129, v61, vcc quad_perm:[1,0,3,2] row_mask:0xf bank_mask:0xf
	global_store_dwordx4 v[136:137], v[130:133], off sc0 sc1 nt
	s_nop 1
	v_pk_mul_f32 v[60:61], v[120:121], v[76:77]
	v_accvgpr_read_b32 v100, a14
	v_mov_b32_e32 v2, v35
	v_accvgpr_mov_b32 a13, a39
	v_accvgpr_write_b32 a20, v22
	v_mov_b32_dpp v11, v80 row_shl:1 row_mask:0xf bank_mask:0xf
	v_pk_fma_f32 v[60:61], v[80:81], v[122:123], v[60:61] op_sel_hi:[0,1,1]
	v_pk_mov_b32 v[62:63], v[80:81], v[100:101] op_sel:[1,0]
	v_mov_b32_dpp v2, v85 row_shr:1 row_mask:0xf bank_mask:0xf
	v_mov_b32_e32 v107, v85
	v_accvgpr_read_b32 v123, a11
	v_accvgpr_write_b32 a21, v23
	v_accvgpr_read_b32 v23, a13
	v_pk_fma_f32 v[60:61], v[62:63], v[10:11], v[60:61]
	v_pk_mul_f32 v[62:63], v[106:107], v[2:3]
	v_accvgpr_read_b32 v122, a10
	v_accvgpr_read_b32 v22, a12
	v_mov_b32_dpp v35, v84 row_shl:1 row_mask:0xf bank_mask:0xf
	v_pk_fma_f32 v[62:63], v[84:85], v[118:119], v[62:63] op_sel_hi:[0,1,1]
	v_accvgpr_write_b32 a12, v118
	v_pk_mov_b32 v[68:69], v[84:85], v[122:123] op_sel:[1,0]
	v_mov_b32_e32 v92, v59
	v_accvgpr_write_b32 a13, v119
	v_pk_fma_f32 v[62:63], v[68:69], v[34:35], v[62:63]
	v_pk_add_f32 v[60:61], v[60:61], 0 op_sel_hi:[1,0]
	v_mov_b32_dpp v92, v117 row_shr:1 row_mask:0xf bank_mask:0xf
	v_mov_b32_e32 v97, v117
	v_mov_b64_e32 v[118:119], v[40:41]
	v_accvgpr_read_b32 v40, a44
	v_pk_add_f32 v[60:61], v[60:61], v[62:63]
	v_pk_mul_f32 v[62:63], v[96:97], v[92:93]
	v_accvgpr_read_b32 v41, a45
	v_mov_b32_dpp v59, v116 row_shl:1 row_mask:0xf bank_mask:0xf
	v_pk_fma_f32 v[62:63], v[116:117], v[118:119], v[62:63] op_sel_hi:[0,1,1]
	v_pk_mov_b32 v[68:69], v[116:117], v[40:41] op_sel:[1,0]
	v_mov_b32_e32 v94, v57
	v_pk_fma_f32 v[62:63], v[68:69], v[58:59], v[62:63]
	s_mov_b64 s[0:1], 0x1020000
	v_pk_add_f32 v[60:61], v[60:61], v[62:63]
	v_mov_b32_dpp v94, v115 row_shr:1 row_mask:0xf bank_mask:0xf
	v_mov_b32_e32 v99, v115
	v_lshl_add_u64 v[62:63], v[54:55], 0, s[0:1]
	v_mov_b32_e32 v128, v60
	v_mov_b32_e32 v129, v61
	v_pk_mul_f32 v[60:61], v[98:99], v[94:95]
	v_mov_b32_e32 v102, v51
	v_accvgpr_write_b32 a30, v4
	v_mov_b32_dpp v57, v114 row_shl:1 row_mask:0xf bank_mask:0xf
	v_pk_fma_f32 v[60:61], v[114:115], v[14:15], v[60:61] op_sel_hi:[0,1,1]
	v_mov_b32_e32 v62, v115
	v_mov_b32_e32 v63, v101
	v_mov_b32_dpp v102, v113 row_shr:1 row_mask:0xf bank_mask:0xf
	v_mov_b32_e32 v105, v113
	v_accvgpr_read_b32 v4, a18
	v_pk_fma_f32 v[60:61], v[62:63], v[56:57], v[60:61]
	v_pk_mul_f32 v[62:63], v[104:105], v[102:103]
	v_accvgpr_read_b32 v5, a19
	v_mov_b32_dpp v51, v112 row_shl:1 row_mask:0xf bank_mask:0xf
	v_pk_fma_f32 v[62:63], v[112:113], v[4:5], v[62:63] op_sel_hi:[0,1,1]
	v_mov_b32_e32 v68, v113
	v_mov_b32_e32 v69, v123
	v_mov_b32_e32 v108, v49
	v_pk_fma_f32 v[62:63], v[68:69], v[50:51], v[62:63]
	v_pk_add_f32 v[60:61], v[60:61], 0 op_sel_hi:[1,0]
	v_mov_b32_dpp v108, v91 row_shr:1 row_mask:0xf bank_mask:0xf
	v_mov_b32_e32 v111, v91
	v_pk_add_f32 v[60:61], v[60:61], v[62:63]
	v_pk_mul_f32 v[62:63], v[110:111], v[108:109]
	v_mov_b32_dpp v49, v90 row_shl:1 row_mask:0xf bank_mask:0xf
	v_pk_fma_f32 v[62:63], v[90:91], v[8:9], v[62:63] op_sel_hi:[0,1,1]
	v_mov_b32_e32 v68, v91
	v_mov_b32_e32 v69, v41
	v_pk_fma_f32 v[62:63], v[68:69], v[48:49], v[62:63]
	s_mov_b64 s[0:1], 0x1030000
	v_pk_add_f32 v[60:61], v[60:61], v[62:63]
	v_lshl_add_u64 v[136:137], v[134:135], 0, s[0:1]
	s_nop 1
	s_mov_b64 vcc, s[28:29]
	s_nop 0
	v_cndmask_b32_dpp v130, v60, v128, vcc quad_perm:[1,0,3,2] row_mask:0xf bank_mask:0xf
	v_cndmask_b32_dpp v131, v61, v129, vcc quad_perm:[1,0,3,2] row_mask:0xf bank_mask:0xf
	s_mov_b64 vcc, s[30:31]
	s_nop 0
	v_cndmask_b32_dpp v132, v128, v60, vcc quad_perm:[1,0,3,2] row_mask:0xf bank_mask:0xf
	v_cndmask_b32_dpp v133, v129, v61, vcc quad_perm:[1,0,3,2] row_mask:0xf bank_mask:0xf
	global_store_dwordx4 v[136:137], v[130:133], off sc0 sc1 nt
	s_nop 1
	s_waitcnt vmcnt(16)
	s_waitcnt lgkmcnt(0)
	s_barrier
	v_accvgpr_read_b32 v2, a0
	v_accvgpr_read_b32 v8, a4
	ds_read_b64 v[60:61], v8
	ds_read_b64 v[62:63], v8 offset:288
	ds_read_b64 v[68:69], v8 offset:576
	ds_read_b64 v[70:71], v8 offset:1728
	ds_read_b64 v[72:73], v8 offset:2016
	ds_read_b64 v[82:83], v8 offset:2304
	ds_read_b64 v[80:81], v8 offset:3456
	ds_read_b64 v[84:85], v8 offset:3744
	ds_read_b64 v[116:117], v8 offset:4032
	ds_read_b64 v[114:115], v8 offset:5184
	ds_read_b64 v[112:113], v8 offset:5472
	ds_read_b64 v[90:91], v8 offset:5760
	ds_read_b32 v43, v2
	ds_read_b32 v19, v2 offset:288
	ds_read_b32 v39, v2 offset:576
	ds_read_b32 v25, v2 offset:1728
	ds_read_b32 v7, v2 offset:2016
	ds_read_b32 v21, v2 offset:2304
	ds_read_b32 v11, v2 offset:3456
	ds_read_b32 v35, v2 offset:3744
	ds_read_b32 v59, v2 offset:4032
	ds_read_b32 v57, v2 offset:5184
	ds_read_b32 v51, v2 offset:5472
	ds_read_b32 v49, v2 offset:5760
	s_waitcnt lgkmcnt(0)
	v_mov_b32_e32 v64, v32
	v_mov_b32_e32 v46, v43
	v_mov_b32_e32 v65, v61
	v_mov_b64_e32 v[100:101], v[22:23]
	v_mov_b32_dpp v46, v61 row_shr:1 row_mask:0xf bank_mask:0xf
	v_pk_mul_f32 v[86:87], v[64:65], v[46:47]
	v_mov_b32_e32 v26, v19
	v_mov_b32_dpp v43, v60 row_shl:1 row_mask:0xf bank_mask:0xf
	v_pk_fma_f32 v[86:87], v[60:61], v[88:89], v[86:87] op_sel_hi:[0,1,1]
	v_pk_mov_b32 v[60:61], v[60:61], v[100:101] op_sel:[1,0]
	v_mov_b32_dpp v26, v63 row_shr:1 row_mask:0xf bank_mask:0xf
	v_mov_b32_e32 v1, v63
	v_accvgpr_read_b32 v67, a35
	v_pk_fma_f32 v[60:61], v[60:61], v[42:43], v[86:87]
	v_pk_mul_f32 v[86:87], v[0:1], v[26:27]
	v_accvgpr_read_b32 v66, a34
	v_accvgpr_write_b32 a10, v14
	v_mov_b32_dpp v19, v62 row_shl:1 row_mask:0xf bank_mask:0xf
	v_pk_fma_f32 v[86:87], v[62:63], v[16:17], v[86:87] op_sel_hi:[0,1,1]
	v_pk_mov_b32 v[62:63], v[62:63], v[66:67] op_sel:[1,0]
	v_mov_b32_e32 v44, v39
	v_accvgpr_write_b32 a11, v15
	v_pk_fma_f32 v[62:63], v[62:63], v[18:19], v[86:87]
	v_pk_add_f32 v[60:61], v[60:61], 0 op_sel_hi:[1,0]
	v_mov_b32_dpp v44, v69 row_shr:1 row_mask:0xf bank_mask:0xf
	v_mov_b32_e32 v31, v69
	v_accvgpr_read_b32 v14, a16
	v_accvgpr_read_b32 v28, a46
	v_pk_add_f32 v[60:61], v[60:61], v[62:63]
	v_pk_mul_f32 v[62:63], v[30:31], v[44:45]
	v_accvgpr_read_b32 v15, a17
	v_accvgpr_read_b32 v29, a47
	v_mov_b32_dpp v39, v68 row_shl:1 row_mask:0xf bank_mask:0xf
	v_pk_fma_f32 v[62:63], v[68:69], v[14:15], v[62:63] op_sel_hi:[0,1,1]
	v_pk_mov_b32 v[68:69], v[68:69], v[28:29] op_sel:[1,0]
	v_mov_b32_e32 v36, v25
	v_pk_fma_f32 v[62:63], v[68:69], v[38:39], v[62:63]
	s_mov_b64 s[0:1], 0x1400000
	v_pk_add_f32 v[60:61], v[60:61], v[62:63]
	v_mov_b32_dpp v36, v71 row_shr:1 row_mask:0xf bank_mask:0xf
	v_mov_b32_e32 v127, v71
	v_accvgpr_read_b32 v8, a20
	v_lshl_add_u64 v[62:63], v[54:55], 0, s[0:1]
	v_mov_b32_e32 v128, v60
	v_mov_b32_e32 v129, v61
	v_pk_mul_f32 v[60:61], v[126:127], v[36:37]
	v_accvgpr_read_b32 v9, a21
	v_accvgpr_write_b32 a25, v23
	v_mov_b32_e32 v12, v7
	v_mov_b32_dpp v25, v70 row_shl:1 row_mask:0xf bank_mask:0xf
	v_pk_fma_f32 v[60:61], v[70:71], v[8:9], v[60:61] op_sel_hi:[0,1,1]
	v_mov_b32_e32 v62, v71
	v_mov_b32_e32 v63, v101
	v_accvgpr_write_b32 a24, v22
	v_mov_b32_dpp v12, v73 row_shr:1 row_mask:0xf bank_mask:0xf
	v_mov_b32_e32 v74, v52
	v_mov_b32_e32 v75, v73
	v_accvgpr_read_b32 v23, a9
	v_accvgpr_write_b32 a26, v124
	v_accvgpr_mov_b32 a2, a22
	v_pk_fma_f32 v[60:61], v[62:63], v[24:25], v[60:61]
	v_pk_mul_f32 v[62:63], v[74:75], v[12:13]
	v_accvgpr_read_b32 v22, a8
	v_accvgpr_write_b32 a27, v125
	v_accvgpr_mov_b32 a3, a23
	v_accvgpr_write_b32 a22, v88
	v_mov_b32_dpp v7, v72 row_shl:1 row_mask:0xf bank_mask:0xf
	v_pk_fma_f32 v[62:63], v[72:73], v[22:23], v[62:63] op_sel_hi:[0,1,1]
	v_mov_b32_e32 v68, v73
	v_mov_b32_e32 v69, v67
	v_mov_b32_e32 v78, v21
	v_accvgpr_write_b32 a23, v89
	v_pk_fma_f32 v[62:63], v[68:69], v[6:7], v[62:63]
	v_pk_add_f32 v[60:61], v[60:61], 0 op_sel_hi:[1,0]
	v_mov_b32_dpp v78, v83 row_shr:1 row_mask:0xf bank_mask:0xf
	v_accvgpr_read_b32 v52, a30
	v_mov_b32_e32 v53, v83
	v_accvgpr_read_b32 v89, a27
	v_pk_add_f32 v[60:61], v[60:61], v[62:63]
	v_pk_mul_f32 v[62:63], v[52:53], v[78:79]
	v_accvgpr_read_b32 v88, a26
	v_mov_b32_dpp v21, v82 row_shl:1 row_mask:0xf bank_mask:0xf
	v_pk_fma_f32 v[62:63], v[82:83], v[88:89], v[62:63] op_sel_hi:[0,1,1]
	v_mov_b32_e32 v68, v83
	v_mov_b32_e32 v69, v29
	v_pk_fma_f32 v[62:63], v[68:69], v[20:21], v[62:63]
	v_mov_b32_e32 v76, v11
	v_accvgpr_read_b32 v125, a37
	v_pk_add_f32 v[60:61], v[60:61], v[62:63]
	s_mov_b64 s[0:1], 0x1410000
	v_mov_b32_dpp v76, v81 row_shr:1 row_mask:0xf bank_mask:0xf
	v_mov_b32_e32 v121, v81
	v_accvgpr_read_b32 v101, a15
	v_accvgpr_read_b32 v124, a36
	v_lshl_add_u64 v[136:137], v[134:135], 0, s[0:1]
	s_nop 1
	s_mov_b64 vcc, s[28:29]
	s_nop 0
	v_cndmask_b32_dpp v130, v60, v128, vcc quad_perm:[1,0,3,2] row_mask:0xf bank_mask:0xf
	v_cndmask_b32_dpp v131, v61, v129, vcc quad_perm:[1,0,3,2] row_mask:0xf bank_mask:0xf
	s_mov_b64 vcc, s[30:31]
	s_nop 0
	v_cndmask_b32_dpp v132, v128, v60, vcc quad_perm:[1,0,3,2] row_mask:0xf bank_mask:0xf
	v_cndmask_b32_dpp v133, v129, v61, vcc quad_perm:[1,0,3,2] row_mask:0xf bank_mask:0xf
	global_store_dwordx4 v[136:137], v[130:133], off sc0 sc1 nt
	s_nop 1
	v_pk_mul_f32 v[60:61], v[120:121], v[76:77]
	v_accvgpr_read_b32 v100, a14
	v_mov_b32_e32 v2, v35
	v_mov_b32_dpp v11, v80 row_shl:1 row_mask:0xf bank_mask:0xf
	v_pk_fma_f32 v[60:61], v[80:81], v[124:125], v[60:61] op_sel_hi:[0,1,1]
	v_pk_mov_b32 v[62:63], v[80:81], v[100:101] op_sel:[1,0]
	v_mov_b32_dpp v2, v85 row_shr:1 row_mask:0xf bank_mask:0xf
	v_mov_b32_e32 v107, v85
	v_accvgpr_read_b32 v29, a13
	v_pk_fma_f32 v[60:61], v[62:63], v[10:11], v[60:61]
	v_pk_mul_f32 v[62:63], v[106:107], v[2:3]
	v_accvgpr_read_b32 v28, a12
	v_mov_b32_dpp v35, v84 row_shl:1 row_mask:0xf bank_mask:0xf
	v_pk_fma_f32 v[62:63], v[84:85], v[28:29], v[62:63] op_sel_hi:[0,1,1]
	v_pk_mov_b32 v[68:69], v[84:85], v[122:123] op_sel:[1,0]
	v_mov_b32_e32 v92, v59
	v_pk_fma_f32 v[62:63], v[68:69], v[34:35], v[62:63]
	v_pk_add_f32 v[60:61], v[60:61], 0 op_sel_hi:[1,0]
	v_mov_b32_dpp v92, v117 row_shr:1 row_mask:0xf bank_mask:0xf
	v_mov_b32_e32 v97, v117
	v_pk_add_f32 v[60:61], v[60:61], v[62:63]
	v_pk_mul_f32 v[62:63], v[96:97], v[92:93]
	v_accvgpr_write_b32 a8, v118
	v_pk_fma_f32 v[62:63], v[116:117], v[118:119], v[62:63] op_sel_hi:[0,1,1]
	v_accvgpr_write_b32 a9, v119
	v_accvgpr_read_b32 v119, a45
	v_accvgpr_read_b32 v118, a44
	v_mov_b32_dpp v59, v116 row_shl:1 row_mask:0xf bank_mask:0xf
	v_pk_mov_b32 v[68:69], v[116:117], v[118:119] op_sel:[1,0]
	v_mov_b32_e32 v94, v57
	v_pk_fma_f32 v[62:63], v[68:69], v[58:59], v[62:63]
	s_mov_b64 s[0:1], 0x1420000
	v_pk_add_f32 v[60:61], v[60:61], v[62:63]
	v_mov_b32_dpp v94, v115 row_shr:1 row_mask:0xf bank_mask:0xf
	v_mov_b32_e32 v99, v115
	v_accvgpr_read_b32 v41, a11
	v_lshl_add_u64 v[62:63], v[54:55], 0, s[0:1]
	v_mov_b32_e32 v128, v60
	v_mov_b32_e32 v129, v61
	v_pk_mul_f32 v[60:61], v[98:99], v[94:95]
	v_accvgpr_read_b32 v40, a10
	v_mov_b32_e32 v102, v51
	v_mov_b32_dpp v57, v114 row_shl:1 row_mask:0xf bank_mask:0xf
	v_pk_fma_f32 v[60:61], v[114:115], v[40:41], v[60:61] op_sel_hi:[0,1,1]
	v_mov_b32_e32 v62, v115
	v_mov_b32_e32 v63, v101
	v_mov_b32_dpp v102, v113 row_shr:1 row_mask:0xf bank_mask:0xf
	v_mov_b32_e32 v105, v113
	v_pk_fma_f32 v[60:61], v[62:63], v[56:57], v[60:61]
	v_pk_mul_f32 v[62:63], v[104:105], v[102:103]
	v_mov_b32_dpp v51, v112 row_shl:1 row_mask:0xf bank_mask:0xf
	v_pk_fma_f32 v[62:63], v[112:113], v[4:5], v[62:63] op_sel_hi:[0,1,1]
	v_mov_b32_e32 v68, v113
	v_mov_b32_e32 v69, v123
	v_mov_b32_e32 v108, v49
	v_pk_fma_f32 v[62:63], v[68:69], v[50:51], v[62:63]
	v_pk_add_f32 v[60:61], v[60:61], 0 op_sel_hi:[1,0]
	v_mov_b32_dpp v108, v91 row_shr:1 row_mask:0xf bank_mask:0xf
	v_mov_b32_e32 v111, v91
	v_accvgpr_read_b32 v5, a3
	v_pk_add_f32 v[60:61], v[60:61], v[62:63]
	v_pk_mul_f32 v[62:63], v[110:111], v[108:109]
	v_accvgpr_read_b32 v4, a2
	v_mov_b32_dpp v49, v90 row_shl:1 row_mask:0xf bank_mask:0xf
	v_pk_fma_f32 v[62:63], v[90:91], v[4:5], v[62:63] op_sel_hi:[0,1,1]
	v_mov_b32_e32 v68, v91
	v_mov_b32_e32 v69, v119
	v_pk_fma_f32 v[62:63], v[68:69], v[48:49], v[62:63]
	s_mov_b64 s[0:1], 0x1430000
	v_pk_add_f32 v[60:61], v[60:61], v[62:63]
	v_lshl_add_u64 v[136:137], v[134:135], 0, s[0:1]
	s_nop 1
	s_mov_b64 vcc, s[28:29]
	s_nop 0
	v_cndmask_b32_dpp v130, v60, v128, vcc quad_perm:[1,0,3,2] row_mask:0xf bank_mask:0xf
	v_cndmask_b32_dpp v131, v61, v129, vcc quad_perm:[1,0,3,2] row_mask:0xf bank_mask:0xf
	s_mov_b64 vcc, s[30:31]
	s_nop 0
	v_cndmask_b32_dpp v132, v128, v60, vcc quad_perm:[1,0,3,2] row_mask:0xf bank_mask:0xf
	v_cndmask_b32_dpp v133, v129, v61, vcc quad_perm:[1,0,3,2] row_mask:0xf bank_mask:0xf
	global_store_dwordx4 v[136:137], v[130:133], off sc0 sc1 nt
	s_nop 1
	s_waitcnt vmcnt(12)
	s_waitcnt lgkmcnt(0)
	s_barrier
	v_accvgpr_read_b32 v2, a1
	v_accvgpr_read_b32 v12, a5
	ds_read_b64 v[60:61], v12
	ds_read_b64 v[62:63], v12 offset:288
	ds_read_b64 v[68:69], v12 offset:576
	ds_read_b64 v[70:71], v12 offset:1728
	ds_read_b64 v[72:73], v12 offset:2016
	ds_read_b64 v[82:83], v12 offset:2304
	ds_read_b64 v[80:81], v12 offset:3456
	ds_read_b64 v[84:85], v12 offset:3744
	ds_read_b64 v[116:117], v12 offset:4032
	ds_read_b64 v[114:115], v12 offset:5184
	ds_read_b64 v[112:113], v12 offset:5472
	ds_read_b64 v[90:91], v12 offset:5760
	ds_read_b32 v43, v2
	ds_read_b32 v19, v2 offset:288
	ds_read_b32 v39, v2 offset:576
	ds_read_b32 v25, v2 offset:1728
	ds_read_b32 v7, v2 offset:2016
	ds_read_b32 v21, v2 offset:2304
	ds_read_b32 v11, v2 offset:3456
	ds_read_b32 v35, v2 offset:3744
	ds_read_b32 v59, v2 offset:4032
	ds_read_b32 v57, v2 offset:5184
	ds_read_b32 v51, v2 offset:5472
	ds_read_b32 v49, v2 offset:5760
	s_waitcnt lgkmcnt(0)
	v_accvgpr_read_b32 v101, a23
	v_mov_b32_e32 v46, v43
	v_mov_b32_e32 v65, v61
	v_accvgpr_read_b32 v31, a25
	v_mov_b32_dpp v46, v61 row_shr:1 row_mask:0xf bank_mask:0xf
	v_pk_mul_f32 v[86:87], v[64:65], v[46:47]
	v_accvgpr_read_b32 v100, a22
	v_accvgpr_read_b32 v30, a24
	v_mov_b32_e32 v26, v19
	v_mov_b32_dpp v43, v60 row_shl:1 row_mask:0xf bank_mask:0xf
	v_pk_fma_f32 v[86:87], v[60:61], v[100:101], v[86:87] op_sel_hi:[0,1,1]
	v_pk_mov_b32 v[60:61], v[60:61], v[30:31] op_sel:[1,0]
	v_mov_b32_dpp v26, v63 row_shr:1 row_mask:0xf bank_mask:0xf
	v_mov_b32_e32 v1, v63
	v_pk_fma_f32 v[60:61], v[60:61], v[42:43], v[86:87]
	v_pk_mul_f32 v[86:87], v[0:1], v[26:27]
	v_accvgpr_read_b32 v0, a34
	v_accvgpr_mov_b32 a12, a14
	v_accvgpr_read_b32 v1, a35
	v_accvgpr_mov_b32 a13, a15
	v_mov_b32_dpp v19, v62 row_shl:1 row_mask:0xf bank_mask:0xf
	v_pk_fma_f32 v[86:87], v[62:63], v[16:17], v[86:87] op_sel_hi:[0,1,1]
	v_accvgpr_write_b32 a14, v16
	v_pk_mov_b32 v[62:63], v[62:63], v[0:1] op_sel:[1,0]
	v_mov_b32_e32 v44, v39
	v_accvgpr_write_b32 a15, v17
	v_pk_fma_f32 v[62:63], v[62:63], v[18:19], v[86:87]
	v_pk_add_f32 v[60:61], v[60:61], 0 op_sel_hi:[1,0]
	v_mov_b32_dpp v44, v69 row_shr:1 row_mask:0xf bank_mask:0xf
	v_accvgpr_read_b32 v16, a48
	v_mov_b32_e32 v17, v69
	v_accvgpr_read_b32 v67, a47
	v_pk_add_f32 v[60:61], v[60:61], v[62:63]
	v_pk_mul_f32 v[62:63], v[16:17], v[44:45]
	v_accvgpr_read_b32 v66, a46
	v_mov_b32_dpp v39, v68 row_shl:1 row_mask:0xf bank_mask:0xf
	v_pk_fma_f32 v[62:63], v[68:69], v[14:15], v[62:63] op_sel_hi:[0,1,1]
	v_pk_mov_b32 v[68:69], v[68:69], v[66:67] op_sel:[1,0]
	v_mov_b32_e32 v36, v25
	v_pk_fma_f32 v[62:63], v[68:69], v[38:39], v[62:63]
	s_mov_b64 s[0:1], 0x1800000
	v_pk_add_f32 v[60:61], v[60:61], v[62:63]
	v_mov_b32_dpp v36, v71 row_shr:1 row_mask:0xf bank_mask:0xf
	v_mov_b32_e32 v127, v71
	v_lshl_add_u64 v[62:63], v[54:55], 0, s[0:1]
	v_mov_b32_e32 v128, v60
	v_mov_b32_e32 v129, v61
	v_pk_mul_f32 v[60:61], v[126:127], v[36:37]
	v_mov_b32_e32 v12, v7
	v_mov_b32_dpp v25, v70 row_shl:1 row_mask:0xf bank_mask:0xf
	v_pk_fma_f32 v[60:61], v[70:71], v[8:9], v[60:61] op_sel_hi:[0,1,1]
	v_mov_b32_e32 v62, v71
	v_mov_b32_e32 v63, v31
	v_mov_b32_dpp v12, v73 row_shr:1 row_mask:0xf bank_mask:0xf
	v_mov_b32_e32 v75, v73
	v_pk_fma_f32 v[60:61], v[62:63], v[24:25], v[60:61]
	v_pk_mul_f32 v[62:63], v[74:75], v[12:13]
	v_mov_b32_dpp v7, v72 row_shl:1 row_mask:0xf bank_mask:0xf
	v_pk_fma_f32 v[62:63], v[72:73], v[22:23], v[62:63] op_sel_hi:[0,1,1]
	v_accvgpr_write_b32 a4, v22
	v_mov_b32_e32 v68, v73
	v_mov_b32_e32 v69, v1
	v_mov_b32_e32 v78, v21
	v_accvgpr_write_b32 a5, v23
	v_pk_fma_f32 v[62:63], v[68:69], v[6:7], v[62:63]
	v_pk_add_f32 v[60:61], v[60:61], 0 op_sel_hi:[1,0]
	v_mov_b32_dpp v78, v83 row_shr:1 row_mask:0xf bank_mask:0xf
	v_mov_b32_e32 v53, v83
	v_accvgpr_read_b32 v22, a26
	v_pk_add_f32 v[60:61], v[60:61], v[62:63]
	v_pk_mul_f32 v[62:63], v[52:53], v[78:79]
	v_accvgpr_read_b32 v23, a27
	v_mov_b32_dpp v21, v82 row_shl:1 row_mask:0xf bank_mask:0xf
	v_pk_fma_f32 v[62:63], v[82:83], v[22:23], v[62:63] op_sel_hi:[0,1,1]
	v_mov_b32_e32 v68, v83
	v_mov_b32_e32 v69, v67
	v_pk_fma_f32 v[62:63], v[68:69], v[20:21], v[62:63]
	v_mov_b32_e32 v76, v11
	v_pk_add_f32 v[60:61], v[60:61], v[62:63]
	s_mov_b64 s[0:1], 0x1810000
	v_mov_b32_dpp v76, v81 row_shr:1 row_mask:0xf bank_mask:0xf
	v_mov_b32_e32 v121, v81
	v_accvgpr_read_b32 v15, a13
	v_lshl_add_u64 v[136:137], v[134:135], 0, s[0:1]
	s_nop 1
	s_mov_b64 vcc, s[28:29]
	s_nop 0
	v_cndmask_b32_dpp v130, v60, v128, vcc quad_perm:[1,0,3,2] row_mask:0xf bank_mask:0xf
	v_cndmask_b32_dpp v131, v61, v129, vcc quad_perm:[1,0,3,2] row_mask:0xf bank_mask:0xf
	s_mov_b64 vcc, s[30:31]
	s_nop 0
	v_cndmask_b32_dpp v132, v128, v60, vcc quad_perm:[1,0,3,2] row_mask:0xf bank_mask:0xf
	v_cndmask_b32_dpp v133, v129, v61, vcc quad_perm:[1,0,3,2] row_mask:0xf bank_mask:0xf
	global_store_dwordx4 v[136:137], v[130:133], off sc0 sc1 nt
	s_nop 1
	v_pk_mul_f32 v[60:61], v[120:121], v[76:77]
	v_accvgpr_read_b32 v14, a12
	v_mov_b32_e32 v2, v35
	v_mov_b32_dpp v11, v80 row_shl:1 row_mask:0xf bank_mask:0xf
	v_pk_fma_f32 v[60:61], v[80:81], v[124:125], v[60:61] op_sel_hi:[0,1,1]
	v_pk_mov_b32 v[62:63], v[80:81], v[14:15] op_sel:[1,0]
	v_mov_b32_dpp v2, v85 row_shr:1 row_mask:0xf bank_mask:0xf
	v_mov_b32_e32 v107, v85
	v_pk_fma_f32 v[60:61], v[62:63], v[10:11], v[60:61]
	v_pk_mul_f32 v[62:63], v[106:107], v[2:3]
	v_mov_b32_dpp v35, v84 row_shl:1 row_mask:0xf bank_mask:0xf
	v_pk_fma_f32 v[62:63], v[84:85], v[28:29], v[62:63] op_sel_hi:[0,1,1]
	v_pk_mov_b32 v[68:69], v[84:85], v[122:123] op_sel:[1,0]
	v_mov_b32_e32 v92, v59
	v_pk_fma_f32 v[62:63], v[68:69], v[34:35], v[62:63]
	v_pk_add_f32 v[60:61], v[60:61], 0 op_sel_hi:[1,0]
	v_mov_b32_dpp v92, v117 row_shr:1 row_mask:0xf bank_mask:0xf
	v_mov_b32_e32 v97, v117
	v_accvgpr_read_b32 v87, a9
	v_pk_add_f32 v[60:61], v[60:61], v[62:63]
	v_pk_mul_f32 v[62:63], v[96:97], v[92:93]
	v_accvgpr_read_b32 v86, a8
	v_mov_b32_dpp v59, v116 row_shl:1 row_mask:0xf bank_mask:0xf
	v_pk_fma_f32 v[62:63], v[116:117], v[86:87], v[62:63] op_sel_hi:[0,1,1]
	v_pk_mov_b32 v[68:69], v[116:117], v[118:119] op_sel:[1,0]
	v_mov_b32_e32 v94, v57
	v_pk_fma_f32 v[62:63], v[68:69], v[58:59], v[62:63]
	s_mov_b64 s[0:1], 0x1820000
	v_pk_add_f32 v[60:61], v[60:61], v[62:63]
	v_mov_b32_dpp v94, v115 row_shr:1 row_mask:0xf bank_mask:0xf
	v_mov_b32_e32 v99, v115
	v_lshl_add_u64 v[62:63], v[54:55], 0, s[0:1]
	v_mov_b32_e32 v128, v60
	v_mov_b32_e32 v129, v61
	v_pk_mul_f32 v[60:61], v[98:99], v[94:95]
	v_mov_b32_e32 v102, v51
	v_mov_b32_dpp v57, v114 row_shl:1 row_mask:0xf bank_mask:0xf
	v_pk_fma_f32 v[60:61], v[114:115], v[40:41], v[60:61] op_sel_hi:[0,1,1]
	v_mov_b32_e32 v62, v115
	v_mov_b32_e32 v63, v15
	v_mov_b32_dpp v102, v113 row_shr:1 row_mask:0xf bank_mask:0xf
	v_mov_b32_e32 v105, v113
	v_accvgpr_read_b32 v89, a19
	v_pk_fma_f32 v[60:61], v[62:63], v[56:57], v[60:61]
	v_pk_mul_f32 v[62:63], v[104:105], v[102:103]
	v_accvgpr_read_b32 v88, a18
	v_mov_b32_dpp v51, v112 row_shl:1 row_mask:0xf bank_mask:0xf
	v_pk_fma_f32 v[62:63], v[112:113], v[88:89], v[62:63] op_sel_hi:[0,1,1]
	v_mov_b32_e32 v68, v113
	v_mov_b32_e32 v69, v123
	v_mov_b32_e32 v108, v49
	v_pk_fma_f32 v[62:63], v[68:69], v[50:51], v[62:63]
	v_pk_add_f32 v[60:61], v[60:61], 0 op_sel_hi:[1,0]
	v_mov_b32_dpp v108, v91 row_shr:1 row_mask:0xf bank_mask:0xf
	v_mov_b32_e32 v111, v91
	v_pk_add_f32 v[60:61], v[60:61], v[62:63]
	v_pk_mul_f32 v[62:63], v[110:111], v[108:109]
	v_mov_b32_dpp v49, v90 row_shl:1 row_mask:0xf bank_mask:0xf
	v_pk_fma_f32 v[62:63], v[90:91], v[4:5], v[62:63] op_sel_hi:[0,1,1]
	v_mov_b32_e32 v68, v91
	v_mov_b32_e32 v69, v119
	v_pk_fma_f32 v[62:63], v[68:69], v[48:49], v[62:63]
	s_mov_b64 s[0:1], 0x1830000
	v_pk_add_f32 v[60:61], v[60:61], v[62:63]
	v_lshl_add_u64 v[136:137], v[134:135], 0, s[0:1]
	s_nop 1
	s_mov_b64 vcc, s[28:29]
	s_nop 0
	v_cndmask_b32_dpp v130, v60, v128, vcc quad_perm:[1,0,3,2] row_mask:0xf bank_mask:0xf
	v_cndmask_b32_dpp v131, v61, v129, vcc quad_perm:[1,0,3,2] row_mask:0xf bank_mask:0xf
	s_mov_b64 vcc, s[30:31]
	s_nop 0
	v_cndmask_b32_dpp v132, v128, v60, vcc quad_perm:[1,0,3,2] row_mask:0xf bank_mask:0xf
	v_cndmask_b32_dpp v133, v129, v61, vcc quad_perm:[1,0,3,2] row_mask:0xf bank_mask:0xf
	global_store_dwordx4 v[136:137], v[130:133], off sc0 sc1 nt
	s_nop 1
	v_accvgpr_write_b32 a12, v28
	s_waitcnt vmcnt(8)
	v_accvgpr_write_b32 a13, v29
	v_mov_b64_e32 v[28:29], v[4:5]
	s_waitcnt lgkmcnt(0)
	s_barrier
	v_accvgpr_read_b32 v2, a6
	v_accvgpr_read_b32 v4, a7
	ds_read_b64 v[60:61], v2
	ds_read_b64 v[62:63], v2 offset:288
	ds_read_b64 v[68:69], v2 offset:576
	ds_read_b64 v[70:71], v2 offset:1728
	ds_read_b64 v[72:73], v2 offset:2016
	ds_read_b64 v[82:83], v2 offset:2304
	ds_read_b64 v[80:81], v2 offset:3456
	ds_read_b64 v[84:85], v2 offset:3744
	ds_read_b64 v[116:117], v2 offset:4032
	ds_read_b64 v[114:115], v2 offset:5184
	ds_read_b64 v[112:113], v2 offset:5472
	ds_read_b64 v[90:91], v2 offset:5760
	ds_read_b32 v43, v4
	ds_read_b32 v19, v4 offset:288
	ds_read_b32 v39, v4 offset:576
	ds_read_b32 v25, v4 offset:1728
	ds_read_b32 v7, v4 offset:2016
	ds_read_b32 v21, v4 offset:2304
	ds_read_b32 v11, v4 offset:3456
	ds_read_b32 v35, v4 offset:3744
	ds_read_b32 v59, v4 offset:4032
	ds_read_b32 v57, v4 offset:5184
	ds_read_b32 v51, v4 offset:5472
	ds_read_b32 v49, v4 offset:5760
	s_waitcnt lgkmcnt(0)
	v_accvgpr_read_b32 v8, a24
	v_mov_b32_e32 v46, v43
	v_mov_b32_e32 v65, v61
	v_mov_b32_e32 v26, v19
	v_mov_b32_dpp v46, v61 row_shr:1 row_mask:0xf bank_mask:0xf
	v_accvgpr_read_b32 v32, a32
	v_accvgpr_read_b32 v9, a25
	v_mov_b64_e32 v[124:125], v[40:41]
	v_pk_mul_f32 v[30:31], v[64:65], v[46:47]
	v_mov_b32_dpp v26, v63 row_shr:1 row_mask:0xf bank_mask:0xf
	v_mov_b32_e32 v33, v63
	v_accvgpr_read_b32 v4, a14
	v_accvgpr_read_b32 v41, a35
	v_mov_b32_e32 v44, v39
	v_pk_fma_f32 v[30:31], v[60:61], v[100:101], v[30:31] op_sel_hi:[0,1,1]
	v_mov_b32_dpp v43, v60 row_shl:1 row_mask:0xf bank_mask:0xf
	v_pk_mov_b32 v[46:47], v[60:61], v[8:9] op_sel:[1,0]
	v_pk_mul_f32 v[26:27], v[32:33], v[26:27]
	v_accvgpr_read_b32 v5, a15
	v_accvgpr_read_b32 v40, a34
	v_mov_b32_dpp v44, v69 row_shr:1 row_mask:0xf bank_mask:0xf
	v_mov_b32_e32 v17, v69
	v_accvgpr_read_b32 v0, a16
	v_pk_fma_f32 v[30:31], v[46:47], v[42:43], v[30:31]
	v_pk_fma_f32 v[26:27], v[62:63], v[4:5], v[26:27] op_sel_hi:[0,1,1]
	v_mov_b32_dpp v19, v62 row_shl:1 row_mask:0xf bank_mask:0xf
	v_pk_mov_b32 v[32:33], v[62:63], v[40:41] op_sel:[1,0]
	v_pk_mul_f32 v[16:17], v[16:17], v[44:45]
	v_accvgpr_read_b32 v1, a17
	v_pk_fma_f32 v[18:19], v[32:33], v[18:19], v[26:27]
	v_pk_add_f32 v[26:27], v[30:31], 0 op_sel_hi:[1,0]
	v_mov_b32_dpp v39, v68 row_shl:1 row_mask:0xf bank_mask:0xf
	v_pk_fma_f32 v[16:17], v[68:69], v[0:1], v[16:17] op_sel_hi:[0,1,1]
	v_pk_mov_b32 v[30:31], v[68:69], v[66:67] op_sel:[1,0]
	v_pk_add_f32 v[18:19], v[26:27], v[18:19]
	v_pk_fma_f32 v[16:17], v[30:31], v[38:39], v[16:17]
	v_mov_b32_e32 v36, v25
	s_mov_b64 s[0:1], 0x1c00000
	v_pk_add_f32 v[16:17], v[18:19], v[16:17]
	v_mov_b32_dpp v36, v71 row_shr:1 row_mask:0xf bank_mask:0xf
	v_mov_b32_e32 v127, v71
	v_accvgpr_read_b32 v0, a20
	v_lshl_add_u64 v[26:27], v[54:55], 0, s[0:1]
	v_mov_b32_e32 v128, v16
	v_mov_b32_e32 v129, v17
	v_mov_b32_e32 v12, v7
	v_pk_mul_f32 v[16:17], v[126:127], v[36:37]
	v_accvgpr_read_b32 v1, a21
	v_mov_b32_dpp v12, v73 row_shr:1 row_mask:0xf bank_mask:0xf
	v_pk_fma_f32 v[16:17], v[70:71], v[0:1], v[16:17] op_sel_hi:[0,1,1]
	v_mov_b32_e32 v75, v73
	v_accvgpr_read_b32 v0, a4
	v_mov_b32_e32 v78, v21
	v_pk_mul_f32 v[12:13], v[74:75], v[12:13]
	v_accvgpr_read_b32 v1, a5
	v_mov_b32_dpp v25, v70 row_shl:1 row_mask:0xf bank_mask:0xf
	v_mov_b32_dpp v7, v72 row_shl:1 row_mask:0xf bank_mask:0xf
	v_mov_b32_dpp v78, v83 row_shr:1 row_mask:0xf bank_mask:0xf
	v_mov_b32_e32 v8, v71
	v_pk_fma_f32 v[12:13], v[72:73], v[0:1], v[12:13] op_sel_hi:[0,1,1]
	v_mov_b32_e32 v5, v41
	v_mov_b32_e32 v4, v73
	v_mov_b32_e32 v53, v83
	v_pk_fma_f32 v[16:17], v[8:9], v[24:25], v[16:17]
	v_pk_fma_f32 v[6:7], v[4:5], v[6:7], v[12:13]
	v_pk_mul_f32 v[12:13], v[52:53], v[78:79]
	v_mov_b32_dpp v21, v82 row_shl:1 row_mask:0xf bank_mask:0xf
	v_pk_add_f32 v[16:17], v[16:17], 0 op_sel_hi:[1,0]
	v_pk_fma_f32 v[12:13], v[82:83], v[22:23], v[12:13] op_sel_hi:[0,1,1]
	v_mov_b32_e32 v66, v83
	v_pk_add_f32 v[6:7], v[16:17], v[6:7]
	v_pk_fma_f32 v[12:13], v[66:67], v[20:21], v[12:13]
	v_mov_b32_e32 v76, v11
	v_pk_add_f32 v[6:7], v[6:7], v[12:13]
	s_mov_b64 s[0:1], 0x1c10000
	v_mov_b32_dpp v76, v81 row_shr:1 row_mask:0xf bank_mask:0xf
	v_mov_b32_e32 v121, v81
	v_accvgpr_read_b32 v0, a36
	v_lshl_add_u64 v[136:137], v[134:135], 0, s[0:1]
	s_nop 1
	s_mov_b64 vcc, s[28:29]
	s_nop 0
	v_cndmask_b32_dpp v130, v6, v128, vcc quad_perm:[1,0,3,2] row_mask:0xf bank_mask:0xf
	v_cndmask_b32_dpp v131, v7, v129, vcc quad_perm:[1,0,3,2] row_mask:0xf bank_mask:0xf
	s_mov_b64 vcc, s[30:31]
	s_nop 0
	v_cndmask_b32_dpp v132, v128, v6, vcc quad_perm:[1,0,3,2] row_mask:0xf bank_mask:0xf
	v_cndmask_b32_dpp v133, v129, v7, vcc quad_perm:[1,0,3,2] row_mask:0xf bank_mask:0xf
	global_store_dwordx4 v[136:137], v[130:133], off sc0 sc1 nt
	s_nop 1
	v_mov_b32_e32 v2, v35
	v_pk_mul_f32 v[6:7], v[120:121], v[76:77]
	v_accvgpr_read_b32 v1, a37
	v_mov_b32_dpp v2, v85 row_shr:1 row_mask:0xf bank_mask:0xf
	v_pk_fma_f32 v[6:7], v[80:81], v[0:1], v[6:7] op_sel_hi:[0,1,1]
	v_mov_b32_e32 v107, v85
	v_accvgpr_read_b32 v0, a12
	v_mov_b32_e32 v92, v59
	v_pk_mul_f32 v[2:3], v[106:107], v[2:3]
	v_accvgpr_read_b32 v1, a13
	v_mov_b32_dpp v11, v80 row_shl:1 row_mask:0xf bank_mask:0xf
	v_mov_b32_dpp v35, v84 row_shl:1 row_mask:0xf bank_mask:0xf
	v_mov_b32_dpp v92, v117 row_shr:1 row_mask:0xf bank_mask:0xf
	v_pk_mov_b32 v[8:9], v[80:81], v[14:15] op_sel:[1,0]
	v_pk_fma_f32 v[2:3], v[84:85], v[0:1], v[2:3] op_sel_hi:[0,1,1]
	v_pk_mov_b32 v[4:5], v[84:85], v[122:123] op_sel:[1,0]
	v_mov_b32_e32 v97, v117
	v_pk_fma_f32 v[6:7], v[8:9], v[10:11], v[6:7]
	v_pk_fma_f32 v[0:1], v[4:5], v[34:35], v[2:3]
	v_pk_mul_f32 v[2:3], v[96:97], v[92:93]
	v_mov_b32_dpp v59, v116 row_shl:1 row_mask:0xf bank_mask:0xf
	v_pk_add_f32 v[6:7], v[6:7], 0 op_sel_hi:[1,0]
	v_pk_fma_f32 v[2:3], v[116:117], v[86:87], v[2:3] op_sel_hi:[0,1,1]
	v_pk_mov_b32 v[4:5], v[116:117], v[118:119] op_sel:[1,0]
	v_pk_add_f32 v[0:1], v[6:7], v[0:1]
	v_pk_fma_f32 v[2:3], v[4:5], v[58:59], v[2:3]
	v_mov_b32_e32 v94, v57
	v_pk_add_f32 v[0:1], v[0:1], v[2:3]
	s_mov_b64 s[0:1], 0x1c20000
	v_mov_b32_dpp v94, v115 row_shr:1 row_mask:0xf bank_mask:0xf
	v_mov_b32_e32 v102, v51
	v_mov_b32_e32 v99, v115
	v_lshl_add_u64 v[2:3], v[54:55], 0, s[0:1]
	v_mov_b32_e32 v128, v0
	v_mov_b32_e32 v129, v1
	v_mov_b32_dpp v102, v113 row_shr:1 row_mask:0xf bank_mask:0xf
	v_pk_mul_f32 v[0:1], v[98:99], v[94:95]
	v_mov_b32_e32 v105, v113
	v_mov_b32_dpp v57, v114 row_shl:1 row_mask:0xf bank_mask:0xf
	v_pk_fma_f32 v[0:1], v[114:115], v[124:125], v[0:1] op_sel_hi:[0,1,1]
	v_mov_b32_e32 v14, v115
	v_pk_mul_f32 v[2:3], v[104:105], v[102:103]
	v_mov_b32_dpp v51, v112 row_shl:1 row_mask:0xf bank_mask:0xf
	v_mov_b32_e32 v108, v49
	v_pk_fma_f32 v[0:1], v[14:15], v[56:57], v[0:1]
	v_pk_fma_f32 v[2:3], v[112:113], v[88:89], v[2:3] op_sel_hi:[0,1,1]
	v_mov_b32_e32 v122, v113
	v_mov_b32_dpp v108, v91 row_shr:1 row_mask:0xf bank_mask:0xf
	v_pk_add_f32 v[0:1], v[0:1], 0 op_sel_hi:[1,0]
	v_pk_fma_f32 v[2:3], v[122:123], v[50:51], v[2:3]
	v_mov_b32_e32 v111, v91
	v_pk_add_f32 v[0:1], v[0:1], v[2:3]
	v_pk_mul_f32 v[2:3], v[110:111], v[108:109]
	v_mov_b32_dpp v49, v90 row_shl:1 row_mask:0xf bank_mask:0xf
	v_pk_fma_f32 v[2:3], v[90:91], v[28:29], v[2:3] op_sel_hi:[0,1,1]
	v_mov_b32_e32 v118, v91
	v_pk_fma_f32 v[2:3], v[118:119], v[48:49], v[2:3]
	s_mov_b64 s[0:1], 0x1c30000
	v_pk_add_f32 v[0:1], v[0:1], v[2:3]
	v_lshl_add_u64 v[136:137], v[134:135], 0, s[0:1]
	s_nop 1
	s_mov_b64 vcc, s[28:29]
	s_nop 0
	v_cndmask_b32_dpp v130, v0, v128, vcc quad_perm:[1,0,3,2] row_mask:0xf bank_mask:0xf
	v_cndmask_b32_dpp v131, v1, v129, vcc quad_perm:[1,0,3,2] row_mask:0xf bank_mask:0xf
	s_mov_b64 vcc, s[30:31]
	s_nop 0
	v_cndmask_b32_dpp v132, v128, v0, vcc quad_perm:[1,0,3,2] row_mask:0xf bank_mask:0xf
	v_cndmask_b32_dpp v133, v129, v1, vcc quad_perm:[1,0,3,2] row_mask:0xf bank_mask:0xf
	global_store_dwordx4 v[136:137], v[130:133], off sc0 sc1 nt
	s_nop 1
	s_endpgm
